# best + leading wave half defers its four K-loop vmcnt(8) waits to the end of the following MFMA block (all five GEMM phases)
# baseline (speedup 1.0000x reference)
;     __device__ __forceinline__ void init(int G_, int c_) { G = G_; c = c_; so.init(M, NPROJ, G_, c_); }
; #define PHASE_BASES() const KAS char* KA = (const KAS char*)__builtin_amdgcn_kernarg_segment_ptr(); asm volatile("" : "+s"(KA)); unsigned char* const ws = *(unsigned char* const KAS*)(KA + 8 * 27)
; #define w_in KARG(8)
; __global__ void __launch_bounds__(NWAVES * 64, 2) mk_fwd(Args args) {
;     ...
;     if (IN(2)) { PHASE_BASES();
;         if ((((bx >> 3) & 15) < 3) || (bx >> 3) == 8) {
;             { constexpr int I_IN = 32 * (PROJ_COLS / 64), NIT = I_IN + 3 * 32 * 32;
;               const MixerCopy Xm{w_in, w_ssd_out, w_sc_out, w_o, ssd_norm_w, WIN, WSSD, WSC, WO};
; #pragma unroll 1
;               for (;;) { int g0 = 0; if (lane == 0) g0 = I_IN + (int)__hip_atomic_fetch_add(ctl + CW_Q4, 8u, __ATOMIC_RELAXED, __HIP_MEMORY_SCOPE_AGENT);
;                   g0 = __builtin_amdgcn_readfirstlane(g0); if (g0 >= NIT) break;
; #pragma unroll 1
;                   for (int k = 0; k < 8; k += 2) wtile_copy_pair(mixer_tile_addr(Xm, g0 + k), mixer_tile_addr(Xm, g0 + k + 1), lane); } }
;             const ExpertCopy X{w_e1, w_e3, w_e2, W13, W2}; expert_copy_share(X, ctl + CW_Q1, lane); }
;         pg8::Gemm g{HX, WIN, MT, NPROJ, D}; OrderProjDyn S; S.init(ctl + CW_QG, MISC + 24, bx);
.LBB0_209:
	v_readfirstlane_b32 s100, v0
	s_lshr_b32 s100, s100, 8
	s_cmp_lt_i32 s78, 3
	s_cselect_b64 s[0:1], -1, 0
	s_cmp_gt_i32 s79, 2
	s_cselect_b64 s[2:3], -1, 0
	s_and_b64 s[0:1], s[0:1], s[2:3]
	s_andn2_b64 vcc, exec, s[0:1]
	s_cbranch_vccnz .LBB0_539
	s_and_b32 s4, s88, 0x78
	s_mov_b64 s[2:3], s[74:75]
	s_cmp_gt_u32 s4, 23
	s_load_dwordx2 s[0:1], s[2:3], 0xd8
	s_cselect_b64 s[4:5], -1, 0
	s_and_b32 s6, s88, -8
	s_cmp_lg_u32 s6, 64
	s_cselect_b64 s[6:7], -1, 0
	s_and_b64 s[4:5], s[4:5], s[6:7]
	s_and_b64 vcc, exec, s[4:5]
	v_and_b32_e32 v130, 48, v0
	s_cbranch_vccnz .LBB0_305
	s_waitcnt lgkmcnt(0)
	s_add_u32 s18, s0, 0x1d200000
	s_load_dwordx2 s[4:5], s[2:3], 0x40
	s_load_dwordx4 s[12:15], s[2:3], 0x70
	s_load_dwordx2 s[10:11], s[2:3], 0x88
	s_load_dwordx2 s[16:17], s[2:3], 0x98
	s_addc_u32 s19, s1, 0
	s_add_u32 s6, s0, 0x1000000
	s_addc_u32 s7, s1, 0
	s_add_u32 s33, s0, 0x1800000
	s_addc_u32 s38, s1, 0
	v_lshlrev_b32_e32 v1, 2, v0
	s_add_u32 s39, s0, 0x2000000
	v_and_b32_e32 v132, 60, v1
	v_lshlrev_b32_e32 v1, 3, v0
	s_addc_u32 s40, s1, 0
	s_mov_b32 s21, 0
	v_cmp_eq_u32_e64 s[8:9], 0, v186
	v_mov_b32_e32 v135, 0
	v_and_b32_e32 v1, 0x78, v1
	v_or_b32_e32 v136, 15, v186
	s_movk_i32 s41, 0x1000
	s_movk_i32 s42, 0x2000
	s_branch .LBB0_214

; #define PG8_STAGE(bufoff, gbase, voff) do { _Pragma("unroll") for (int _i = 0; _i < 2; ++_i) \
;         __builtin_amdgcn_global_load_lds((const unsigned*)((const char*)(gbase) + (voff)[_i]), (PG8_LAS unsigned*)(lds + (bufoff) + ldsw + _i * 8192), 16, 0, 0); } while (0)
; #define PG8_LDA(dst, b, h) do { _Pragma("unroll") for (int m = 0; m < 4; ++m) _Pragma("unroll") for (int k = 0; k < 2; ++k) dst[m][k] = *(const PG8_LAS bf16x8*)(lds + PG8_SA(b, h) + aoff + m * 2048 + k * 1024); } while (0)
; #define PG8_LDB(dst, b, h) do { _Pragma("unroll") for (int n = 0; n < 2; ++n) _Pragma("unroll") for (int k = 0; k < 2; ++k) dst[n][k] = *(const PG8_LAS bf16x8*)(lds + PG8_SB(b, h) + boff + n * 2048 + k * 1024); } while (0)
; #define PG8_MMA(ai, bj, At, Bt) do { __builtin_amdgcn_s_setprio(1); _Pragma("unroll") for (int m = 0; m < 4; ++m) _Pragma("unroll") for (int n = 0; n < 2; ++n) _Pragma("unroll") for (int k = 0; k < 2; ++k) \
;         acc[ai][bj][m][n] = __builtin_amdgcn_mfma_f32_16x16x32_bf16(Bt[n][k], At[m][k], acc[ai][bj][m][n], 0, 0, 0); __builtin_amdgcn_s_setprio(0); } while (0)
; #define PG8_WAIT_V(n) asm volatile("s_waitcnt vmcnt(" #n ")" ::: "memory")
; #define PG8_WAIT_L(n) asm volatile("s_waitcnt lgkmcnt(" #n ")" ::: "memory")
; #define PG8_BAR __builtin_amdgcn_s_barrier()
; #define PG8_SCHED __builtin_amdgcn_sched_barrier(0)
; #define PG8_STAGE(bufoff, gbase, voff) do { _Pragma("unroll") for (int _i = 0; _i < 2; ++_i) \
;         __builtin_amdgcn_global_load_lds((const unsigned*)((const char*)(gbase) + (voff)[_i]), (PG8_LAS unsigned*)(lds + (bufoff) + ldsw + _i * 8192), 16, 0, 0); } while (0)
; #define PG8_LDA(dst, b, h) do { _Pragma("unroll") for (int m = 0; m < 4; ++m) _Pragma("unroll") for (int k = 0; k < 2; ++k) dst[m][k] = *(const PG8_LAS bf16x8*)(lds + PG8_SA(b, h) + aoff + m * 2048 + k * 1024); } while (0)
; #define PG8_WAIT_V(n) asm volatile("s_waitcnt vmcnt(" #n ")" ::: "memory")
; template <class Epi, class Sched, bool ALIGN_EPI = false, bool SP2 = false>
; __device__ __forceinline__ void gemm_phase(PG8_LAS unsigned char* lds, const Gemm g, const Sched& S, const Epi& E) {
;     ...
;             PG8_LDB(B0, 0, 0); PG8_LDB(B1, 0, 1); PG8_SCHED; PG8_LDA(At, 0, 0); PG8_STAGE(PG8_SA(1, 1), a1 + hstep, voffA);
;             PG8_WAIT_V(8); PG8_WAIT_L(0); PG8_BAR; PG8_MMA(0, 0, At, B0); PG8_MMA(0, 1, At, B1); PG8_BAR; PG8_SCHED;
.LBB0_332:
	ds_read_b128 v[132:135], v213
	ds_read_b128 v[136:139], v213 offset:1024
	ds_read_b128 v[140:143], v213 offset:2048
	ds_read_b128 v[144:147], v213 offset:3072
	ds_read_b128 v[148:151], v214
	ds_read_b128 v[152:155], v214 offset:1024
	ds_read_b128 v[156:159], v214 offset:2048
	ds_read_b128 v[178:181], v214 offset:3072
	s_add_u32 s2, s0, 0xfff80080
	s_addc_u32 s3, s1, -1
	s_cmp_eq_u32 s95, 28
	s_cselect_b32 s5, s7, s3
	s_cselect_b32 s4, s33, s2
	s_cselect_b32 s3, s53, s85
	s_cselect_b32 s2, s55, s84
	v_lshl_add_u64 v[160:161], s[0:1], 0, v[172:173]
	s_add_i32 m0, s63, 0xc000
	ds_read_b128 v[182:185], v215
	ds_read_b128 v[188:191], v215 offset:1024
	ds_read_b128 v[192:195], v215 offset:2048
	ds_read_b128 v[196:199], v215 offset:3072
	ds_read_b128 v[200:203], v215 offset:4096
	ds_read_b128 v[204:207], v215 offset:5120
	ds_read_b128 v[218:221], v215 offset:6144
	ds_read_b128 v[222:225], v215 offset:7168
	global_load_lds_dwordx4 v[160:161], off
	v_lshl_add_u64 v[160:161], s[0:1], 0, v[174:175]
	s_add_i32 m0, s63, 0xe000
	s_nop 0
	global_load_lds_dwordx4 v[160:161], off
	s_cmp_eq_u32 s100, 0
	s_cbranch_scc1 .Lllw2_a0
	s_waitcnt vmcnt(8)
.Lllw2_a0:
	s_waitcnt lgkmcnt(0)
	s_barrier
	s_setprio 1
	s_waitcnt lgkmcnt(0)
	v_mfma_f32_16x16x32_bf16 v[126:129], v[132:135], v[182:185], v[126:129]
	v_mfma_f32_16x16x32_bf16 v[122:125], v[140:143], v[182:185], v[122:125]
	v_mfma_f32_16x16x32_bf16 v[118:121], v[132:135], v[192:195], v[118:121]
	v_mfma_f32_16x16x32_bf16 v[110:113], v[140:143], v[192:195], v[110:113]
	v_mfma_f32_16x16x32_bf16 v[102:105], v[132:135], v[200:203], v[102:105]
	v_mfma_f32_16x16x32_bf16 v[94:97], v[140:143], v[200:203], v[94:97]
	v_mfma_f32_16x16x32_bf16 v[86:89], v[132:135], v[218:221], v[86:89]
	v_mfma_f32_16x16x32_bf16 v[78:81], v[140:143], v[218:221], v[78:81]
	v_mfma_f32_16x16x32_bf16 v[126:129], v[136:139], v[188:191], v[126:129]
	v_mfma_f32_16x16x32_bf16 v[122:125], v[144:147], v[188:191], v[122:125]
	v_mfma_f32_16x16x32_bf16 v[118:121], v[136:139], v[196:199], v[118:121]
	v_mfma_f32_16x16x32_bf16 v[110:113], v[144:147], v[196:199], v[110:113]
	v_mfma_f32_16x16x32_bf16 v[102:105], v[136:139], v[204:207], v[102:105]
	v_mfma_f32_16x16x32_bf16 v[94:97], v[144:147], v[204:207], v[94:97]
	v_mfma_f32_16x16x32_bf16 v[86:89], v[136:139], v[222:225], v[86:89]
	v_mfma_f32_16x16x32_bf16 v[78:81], v[144:147], v[222:225], v[78:81]
	s_setprio 0
	s_setprio 1
	v_mfma_f32_16x16x32_bf16 v[114:117], v[148:151], v[182:185], v[114:117]
	v_mfma_f32_16x16x32_bf16 v[106:109], v[156:159], v[182:185], v[106:109]
	v_mfma_f32_16x16x32_bf16 v[98:101], v[148:151], v[192:195], v[98:101]
	v_mfma_f32_16x16x32_bf16 v[90:93], v[156:159], v[192:195], v[90:93]
	v_mfma_f32_16x16x32_bf16 v[82:85], v[148:151], v[200:203], v[82:85]
	v_mfma_f32_16x16x32_bf16 v[74:77], v[156:159], v[200:203], v[74:77]
	v_mfma_f32_16x16x32_bf16 v[70:73], v[148:151], v[218:221], v[70:73]
	v_mfma_f32_16x16x32_bf16 v[66:69], v[156:159], v[218:221], v[66:69]
	v_mfma_f32_16x16x32_bf16 v[114:117], v[152:155], v[188:191], v[114:117]
	v_mfma_f32_16x16x32_bf16 v[106:109], v[178:181], v[188:191], v[106:109]
	v_mfma_f32_16x16x32_bf16 v[98:101], v[152:155], v[196:199], v[98:101]
	v_mfma_f32_16x16x32_bf16 v[90:93], v[178:181], v[196:199], v[90:93]
	v_mfma_f32_16x16x32_bf16 v[82:85], v[152:155], v[204:207], v[82:85]
	v_mfma_f32_16x16x32_bf16 v[74:77], v[178:181], v[204:207], v[74:77]
	v_mfma_f32_16x16x32_bf16 v[70:73], v[152:155], v[222:225], v[70:73]
	v_mfma_f32_16x16x32_bf16 v[66:69], v[178:181], v[222:225], v[66:69]
	s_setprio 0
	s_cmp_lg_u32 s100, 0
	s_cbranch_scc1 .Lllw2_b0
	s_waitcnt vmcnt(8)
; #define PG8_STAGE(bufoff, gbase, voff) do { _Pragma("unroll") for (int _i = 0; _i < 2; ++_i) \
;         __builtin_amdgcn_global_load_lds((const unsigned*)((const char*)(gbase) + (voff)[_i]), (PG8_LAS unsigned*)(lds + (bufoff) + ldsw + _i * 8192), 16, 0, 0); } while (0)
; #define PG8_LDA(dst, b, h) do { _Pragma("unroll") for (int m = 0; m < 4; ++m) _Pragma("unroll") for (int k = 0; k < 2; ++k) dst[m][k] = *(const PG8_LAS bf16x8*)(lds + PG8_SA(b, h) + aoff + m * 2048 + k * 1024); } while (0)
; #define PG8_LDB(dst, b, h) do { _Pragma("unroll") for (int n = 0; n < 2; ++n) _Pragma("unroll") for (int k = 0; k < 2; ++k) dst[n][k] = *(const PG8_LAS bf16x8*)(lds + PG8_SB(b, h) + boff + n * 2048 + k * 1024); } while (0)
; #define PG8_MMA(ai, bj, At, Bt) do { __builtin_amdgcn_s_setprio(1); _Pragma("unroll") for (int m = 0; m < 4; ++m) _Pragma("unroll") for (int n = 0; n < 2; ++n) _Pragma("unroll") for (int k = 0; k < 2; ++k) \
;         acc[ai][bj][m][n] = __builtin_amdgcn_mfma_f32_16x16x32_bf16(Bt[n][k], At[m][k], acc[ai][bj][m][n], 0, 0, 0); __builtin_amdgcn_s_setprio(0); } while (0)
; #define PG8_WAIT_V(n) asm volatile("s_waitcnt vmcnt(" #n ")" ::: "memory")
; #define PG8_WAIT_L(n) asm volatile("s_waitcnt lgkmcnt(" #n ")" ::: "memory")
; #define PG8_BAR __builtin_amdgcn_s_barrier()
; #define PG8_SCHED __builtin_amdgcn_sched_barrier(0)
; #define PG8_STAGE(bufoff, gbase, voff) do { _Pragma("unroll") for (int _i = 0; _i < 2; ++_i) \
;         __builtin_amdgcn_global_load_lds((const unsigned*)((const char*)(gbase) + (voff)[_i]), (PG8_LAS unsigned*)(lds + (bufoff) + ldsw + _i * 8192), 16, 0, 0); } while (0)
; #define PG8_BAR __builtin_amdgcn_s_barrier()
; template <class Epi, class Sched, bool ALIGN_EPI = false, bool SP2 = false>
; __device__ __forceinline__ void gemm_phase(PG8_LAS unsigned char* lds, const Gemm g, const Sched& S, const Epi& E) {
;     ...
;             PG8_WAIT_V(8); PG8_WAIT_L(0); PG8_BAR; PG8_MMA(0, 0, At, B0); PG8_MMA(0, 1, At, B1); PG8_BAR; PG8_SCHED;
;             PG8_LDA(At, 0, 1); PG8_STAGE(PG8_SB(0, 0), b2, voffB); PG8_STAGE(PG8_SB(0, 1), b2 + hstep, voffB); PG8_STAGE(PG8_SA(0, 0), a2, voffA);
;             PG8_WAIT_V(8); PG8_WAIT_L(0); PG8_BAR; PG8_MMA(1, 0, At, B0); PG8_MMA(1, 1, At, B1); PG8_BAR; PG8_SCHED;
;             PG8_LDB(B0, 1, 0); PG8_LDB(B1, 1, 1); PG8_SCHED; PG8_LDA(At, 1, 0); PG8_STAGE(PG8_SA(0, 1), a2 + hstep, voffA);
.Lllw2_b0:
	s_barrier
	s_add_i32 s96, s81, s66
	v_lshl_add_u64 v[160:161], s[2:3], 0, v[164:165]
	s_mov_b32 m0, s96
	ds_read_b128 v[182:185], v215 offset:16384
	ds_read_b128 v[188:191], v215 offset:17408
	ds_read_b128 v[192:195], v215 offset:18432
	ds_read_b128 v[196:199], v215 offset:19456
	ds_read_b128 v[200:203], v215 offset:20480
	ds_read_b128 v[204:207], v215 offset:21504
	ds_read_b128 v[218:221], v215 offset:22528
	ds_read_b128 v[222:225], v215 offset:23552
	global_load_lds_dwordx4 v[160:161], off
	s_add_i32 m0, s96, 0x2000
	s_add_u32 s96, s2, 0x80000
	v_lshl_add_u64 v[208:209], s[2:3], 0, v[168:169]
	s_addc_u32 s97, s3, 0
	s_add_i32 vcc_lo, s82, s66
	global_load_lds_dwordx4 v[208:209], off
	v_lshl_add_u64 v[226:227], s[96:97], 0, v[164:165]
	s_mov_b32 m0, vcc_lo
	v_lshl_add_u64 v[228:229], s[4:5], 0, v[166:167]
	global_load_lds_dwordx4 v[226:227], off
	v_lshl_add_u64 v[226:227], s[96:97], 0, v[168:169]
	s_add_i32 m0, vcc_lo, 0x2000
	s_nop 0
	global_load_lds_dwordx4 v[226:227], off
	v_lshl_add_u64 v[226:227], s[4:5], 0, v[162:163]
	s_mov_b32 m0, s63
	s_nop 0
	global_load_lds_dwordx4 v[226:227], off
	s_mov_b32 m0, s65
	s_nop 0
	global_load_lds_dwordx4 v[228:229], off
	s_cmp_eq_u32 s100, 0
	s_cbranch_scc1 .Lllw2_a1
	s_waitcnt vmcnt(8)
.Lllw2_a1:
	s_waitcnt lgkmcnt(0)
	s_barrier
	s_setprio 1
	s_waitcnt lgkmcnt(0)
	v_mfma_f32_16x16x32_bf16 v[62:65], v[132:135], v[182:185], v[62:65]
	v_mfma_f32_16x16x32_bf16 v[58:61], v[140:143], v[182:185], v[58:61]
	v_mfma_f32_16x16x32_bf16 v[54:57], v[132:135], v[192:195], v[54:57]
	v_mfma_f32_16x16x32_bf16 v[46:49], v[140:143], v[192:195], v[46:49]
	v_mfma_f32_16x16x32_bf16 v[38:41], v[132:135], v[200:203], v[38:41]
	v_mfma_f32_16x16x32_bf16 v[30:33], v[140:143], v[200:203], v[30:33]
	v_mfma_f32_16x16x32_bf16 v[22:25], v[132:135], v[218:221], v[22:25]
	v_mfma_f32_16x16x32_bf16 v[14:17], v[140:143], v[218:221], v[14:17]
	v_mfma_f32_16x16x32_bf16 v[62:65], v[136:139], v[188:191], v[62:65]
	v_mfma_f32_16x16x32_bf16 v[58:61], v[144:147], v[188:191], v[58:61]
	v_mfma_f32_16x16x32_bf16 v[54:57], v[136:139], v[196:199], v[54:57]
	v_mfma_f32_16x16x32_bf16 v[46:49], v[144:147], v[196:199], v[46:49]
	v_mfma_f32_16x16x32_bf16 v[38:41], v[136:139], v[204:207], v[38:41]
	v_mfma_f32_16x16x32_bf16 v[30:33], v[144:147], v[204:207], v[30:33]
	v_mfma_f32_16x16x32_bf16 v[22:25], v[136:139], v[222:225], v[22:25]
	v_mfma_f32_16x16x32_bf16 v[14:17], v[144:147], v[222:225], v[14:17]
	s_setprio 0
	s_setprio 1
	v_mfma_f32_16x16x32_bf16 v[50:53], v[148:151], v[182:185], v[50:53]
	v_mfma_f32_16x16x32_bf16 v[42:45], v[156:159], v[182:185], v[42:45]
	v_mfma_f32_16x16x32_bf16 v[34:37], v[148:151], v[192:195], v[34:37]
	v_mfma_f32_16x16x32_bf16 v[26:29], v[156:159], v[192:195], v[26:29]
	v_mfma_f32_16x16x32_bf16 v[18:21], v[148:151], v[200:203], v[18:21]
	v_mfma_f32_16x16x32_bf16 v[10:13], v[156:159], v[200:203], v[10:13]
	v_mfma_f32_16x16x32_bf16 v[6:9], v[148:151], v[218:221], v[6:9]
	v_mfma_f32_16x16x32_bf16 v[2:5], v[156:159], v[218:221], v[2:5]
	v_mfma_f32_16x16x32_bf16 v[50:53], v[152:155], v[188:191], v[50:53]
	v_mfma_f32_16x16x32_bf16 v[42:45], v[178:181], v[188:191], v[42:45]
	v_mfma_f32_16x16x32_bf16 v[34:37], v[152:155], v[196:199], v[34:37]
	v_mfma_f32_16x16x32_bf16 v[26:29], v[178:181], v[196:199], v[26:29]
	v_mfma_f32_16x16x32_bf16 v[18:21], v[152:155], v[204:207], v[18:21]
	v_mfma_f32_16x16x32_bf16 v[10:13], v[178:181], v[204:207], v[10:13]
	v_mfma_f32_16x16x32_bf16 v[6:9], v[152:155], v[222:225], v[6:9]
	v_mfma_f32_16x16x32_bf16 v[2:5], v[178:181], v[222:225], v[2:5]
	s_setprio 0
	s_cmp_lg_u32 s100, 0
	s_cbranch_scc1 .Lllw2_b1
	s_waitcnt vmcnt(8)
.Lllw2_b1:
	s_barrier
	s_add_i32 s96, 0, 0x18000
	v_add_u32_e32 v131, s96, v211
	s_add_i32 s97, 0, 0x1c000
	ds_read_b128 v[132:135], v131
	ds_read_b128 v[136:139], v131 offset:1024
	ds_read_b128 v[140:143], v131 offset:2048
	ds_read_b128 v[144:147], v131 offset:3072
	v_add_u32_e32 v131, s97, v211
	ds_read_b128 v[148:151], v131
	ds_read_b128 v[152:155], v131 offset:1024
	ds_read_b128 v[156:159], v131 offset:2048
	ds_read_b128 v[178:181], v131 offset:3072
	s_add_u32 s4, s4, 0x80000
	s_addc_u32 s5, s5, 0
	s_mov_b32 m0, s71
	v_lshl_add_u64 v[230:231], s[4:5], 0, v[162:163]
	ds_read_b128 v[182:185], v215 offset:32768
	ds_read_b128 v[188:191], v215 offset:33792
	ds_read_b128 v[192:195], v215 offset:34816
	ds_read_b128 v[196:199], v215 offset:35840
	ds_read_b128 v[200:203], v215 offset:36864
	ds_read_b128 v[204:207], v215 offset:37888
	ds_read_b128 v[218:221], v215 offset:38912
	ds_read_b128 v[222:225], v215 offset:39936
	global_load_lds_dwordx4 v[230:231], off
	v_lshl_add_u64 v[230:231], s[4:5], 0, v[166:167]
	s_mov_b32 m0, s72
	s_nop 0
	global_load_lds_dwordx4 v[230:231], off
	s_cmp_eq_u32 s100, 0
	s_cbranch_scc1 .Lllw2_a2
	s_waitcnt vmcnt(8)

; #define PG8_STAGE(bufoff, gbase, voff) do { _Pragma("unroll") for (int _i = 0; _i < 2; ++_i) \
;         __builtin_amdgcn_global_load_lds((const unsigned*)((const char*)(gbase) + (voff)[_i]), (PG8_LAS unsigned*)(lds + (bufoff) + ldsw + _i * 8192), 16, 0, 0); } while (0)
; #define PG8_LDA(dst, b, h) do { _Pragma("unroll") for (int m = 0; m < 4; ++m) _Pragma("unroll") for (int k = 0; k < 2; ++k) dst[m][k] = *(const PG8_LAS bf16x8*)(lds + PG8_SA(b, h) + aoff + m * 2048 + k * 1024); } while (0)
; #define PG8_MMA(ai, bj, At, Bt) do { __builtin_amdgcn_s_setprio(1); _Pragma("unroll") for (int m = 0; m < 4; ++m) _Pragma("unroll") for (int n = 0; n < 2; ++n) _Pragma("unroll") for (int k = 0; k < 2; ++k) \
;         acc[ai][bj][m][n] = __builtin_amdgcn_mfma_f32_16x16x32_bf16(Bt[n][k], At[m][k], acc[ai][bj][m][n], 0, 0, 0); __builtin_amdgcn_s_setprio(0); } while (0)
; #define PG8_WAIT_V(n) asm volatile("s_waitcnt vmcnt(" #n ")" ::: "memory")
; #define PG8_WAIT_L(n) asm volatile("s_waitcnt lgkmcnt(" #n ")" ::: "memory")
; #define PG8_BAR __builtin_amdgcn_s_barrier()
; #define PG8_SCHED __builtin_amdgcn_sched_barrier(0)
; #define PG8_STAGE(bufoff, gbase, voff) do { _Pragma("unroll") for (int _i = 0; _i < 2; ++_i) \
;         __builtin_amdgcn_global_load_lds((const unsigned*)((const char*)(gbase) + (voff)[_i]), (PG8_LAS unsigned*)(lds + (bufoff) + ldsw + _i * 8192), 16, 0, 0); } while (0)
; #define PG8_LDA(dst, b, h) do { _Pragma("unroll") for (int m = 0; m < 4; ++m) _Pragma("unroll") for (int k = 0; k < 2; ++k) dst[m][k] = *(const PG8_LAS bf16x8*)(lds + PG8_SA(b, h) + aoff + m * 2048 + k * 1024); } while (0)
; #define PG8_WAIT_V(n) asm volatile("s_waitcnt vmcnt(" #n ")" ::: "memory")
; #define PG8_WAIT_L(n) asm volatile("s_waitcnt lgkmcnt(" #n ")" ::: "memory")
; #define PG8_BAR __builtin_amdgcn_s_barrier()
; #define PG8_SCHED __builtin_amdgcn_sched_barrier(0)
; template <class Epi, class Sched, bool ALIGN_EPI = false, bool SP2 = false>
; __device__ __forceinline__ void gemm_phase(PG8_LAS unsigned char* lds, const Gemm g, const Sched& S, const Epi& E) {
;     ...
;             PG8_LDA(At, 1, 1); PG8_STAGE(PG8_SB(1, 0), b3, voffB); PG8_STAGE(PG8_SB(1, 1), b3 + hstep, voffB); PG8_STAGE(PG8_SA(1, 0), a3, voffA);
;             PG8_WAIT_V(8); PG8_WAIT_L(0); PG8_BAR; PG8_MMA(1, 0, At, B0); PG8_MMA(1, 1, At, B1); PG8_BAR; PG8_SCHED;
.Lllw2_b2:
	s_barrier
	s_add_i32 s4, s96, s66
	v_lshl_add_u64 v[160:161], v[160:161], 0, s[40:41]
	s_mov_b32 m0, s4
	ds_read_b128 v[182:185], v215 offset:49152
	ds_read_b128 v[188:191], v215 offset:50176
	ds_read_b128 v[192:195], v215 offset:51200
	ds_read_b128 v[196:199], v215 offset:52224
	ds_read_b128 v[200:203], v215 offset:53248
	ds_read_b128 v[204:207], v215 offset:54272
	ds_read_b128 v[218:221], v215 offset:55296
	ds_read_b128 v[222:225], v215 offset:56320
	global_load_lds_dwordx4 v[160:161], off
	s_add_i32 m0, s4, 0x2000
	s_add_u32 s2, s2, 0x80080
	v_lshl_add_u64 v[160:161], v[208:209], 0, s[40:41]
	s_addc_u32 s3, s3, 0
	s_add_i32 s4, s97, s66
	global_load_lds_dwordx4 v[160:161], off
	v_lshl_add_u64 v[160:161], s[2:3], 0, v[164:165]
	s_mov_b32 m0, s4
	s_nop 0
	global_load_lds_dwordx4 v[160:161], off
	v_lshl_add_u64 v[160:161], s[2:3], 0, v[168:169]
	s_add_i32 m0, s4, 0x2000
	s_nop 0
	global_load_lds_dwordx4 v[160:161], off
	v_lshl_add_u64 v[160:161], v[226:227], 0, s[40:41]
	s_mov_b32 m0, s74
	s_nop 0
	global_load_lds_dwordx4 v[160:161], off
	v_lshl_add_u64 v[160:161], v[228:229], 0, s[40:41]
	s_mov_b32 m0, s75
	s_nop 0
	global_load_lds_dwordx4 v[160:161], off
	s_cmp_eq_u32 s100, 0
	s_cbranch_scc1 .Lllw2_a3
	s_waitcnt vmcnt(8)

; #define PG8_BAR __builtin_amdgcn_s_barrier()
; #define PG8_BAR __builtin_amdgcn_s_barrier()
;     __device__ __forceinline__ void claim_publish(int i, unsigned r, int wid, int lane) const { const unsigned rr = __builtin_amdgcn_readfirstlane(r); if (lane == 0) slot[wid == 0 ? (i & 3) : 4 + wid] = rr; asm volatile("s_waitcnt lgkmcnt(0)" ::: "memory"); }
; template <class Epi, class Sched, bool ALIGN_EPI = false, bool SP2 = false>
; __device__ __forceinline__ void gemm_phase(PG8_LAS unsigned char* lds, const Gemm g, const Sched& S, const Epi& E) {
;     ...
;         if constexpr (Sched::DYNAMIC) { static_assert(!Sched::DYNAMIC || ALIGN_EPI, "dynamic orders publish in front of the ALIGN_EPI barrier"); S.claim_publish(ui + 2, pend, wid, lane); }
;         if constexpr (ALIGN_EPI) { if (wr == 0) PG8_BAR; }
.Lllw2_b3:
	s_barrier
	s_add_i32 s95, s95, 2
	s_add_u32 s0, s0, 0x100
	s_addc_u32 s1, s1, 0
	s_add_u32 s84, s84, 0x100
	s_addc_u32 s85, s85, 0
	s_cmp_gt_u32 s95, 29
	s_cbranch_scc0 .LBB0_332
	s_waitcnt vmcnt(0)
	v_readfirstlane_b32 s2, v130
	s_and_saveexec_b64 s[0:1], s[10:11]
	s_cbranch_execz .LBB0_335
	s_and_b32 s3, s6, 3
	s_xor_b32 s3, s3, 2
	s_and_b64 s[4:5], s[42:43], exec
	s_cselect_b32 s3, s3, s76
	s_lshl_b32 s3, s3, 2
	s_add_i32 s3, s3, 0
	s_add_i32 s3, s3, 0x27da0
	v_mov_b32_e32 v130, s3
	v_mov_b32_e32 v131, s2
	ds_write_b32 v130, v131

;     __device__ __forceinline__ void init(int G_, int c_) { G = G_; c = c_; so.init(M, NPROJ, G_, c_); }
;     __device__ __forceinline__ bool next(int i, pg8::Unit& u) const { const int s = i >= R ? 1 : 0; const bool ok = so.next(i - s * R, u); u.sel = s; return ok && i < 2 * R; }
; #define PHASE_BASES() const KAS char* KA = (const KAS char*)__builtin_amdgcn_kernarg_segment_ptr(); asm volatile("" : "+s"(KA)); unsigned char* const ws = *(unsigned char* const KAS*)(KA + 8 * 27)
;     __host__ __device__ __forceinline__ bool next(int i, Unit& u) const {
;         const long L = (long)i * G + c; if (L >= nwg) return false;
;         int wgid = (int)L; { const int q = nwg / NXCD, r = nwg % NXCD, xcd = wgid % NXCD, off = wgid / NXCD; wgid = (xcd < r ? xcd * (q + 1) : r * (q + 1) + (xcd - r) * q) + off; }
;         const int nig = WGM * nN, gid = wgid / nig, fm = gid * WGM, gsz = (nM - fm) < WGM ? (nM - fm) : WGM;
;         u.pm = fm + ((wgid % nig) % gsz); u.pn = (wgid % nig) / gsz; return true;
; __global__ void __launch_bounds__(NWAVES * 64, 2) mk_fwd(Args args) {
;     ...
;     if (IN(6)) { PHASE_BASES();
;         { pg8::Gemm g{Yn, WSSD, M, D, D, SCY, WSC}; OrderTwice S; S.so.init(M, D, G, bx); S.R = (512 + G - 1) / G; EpiGate E{Gt, b_gate, MERGED};
;           pg8::gemm_phase<EpiGate, OrderTwice, true, true>(lds, g, S, E); }
.LBB0_880:
	v_readfirstlane_b32 s100, v0
	s_lshr_b32 s100, s100, 8
	s_cmp_lt_i32 s78, 7
	s_cselect_b64 s[0:1], -1, 0
	s_cmp_gt_i32 s79, 6
	s_cselect_b64 s[2:3], -1, 0
	s_and_b64 s[0:1], s[0:1], s[2:3]
	s_andn2_b64 vcc, exec, s[0:1]
	s_cbranch_vccnz .LBB0_993
	s_abs_i32 s0, s86
	v_cvt_f32_u32_e32 v1, s0
	s_sub_i32 s5, 0, s0
	s_add_i32 s1, s86, 0x1ff
	s_xor_b32 s4, s1, s86
	v_rcp_iflag_f32_e32 v1, v1
	s_abs_i32 s1, s1
	s_ashr_i32 s4, s4, 31
	s_mov_b64 s[2:3], s[74:75]
	v_mul_f32_e32 v1, 0x4f7ffffe, v1
	v_cvt_u32_f32_e32 v1, v1
	v_mov_b64_e32 v[2:3], 0x200
	v_readfirstlane_b32 s12, v0
	v_readfirstlane_b32 s6, v1
	s_mul_i32 s5, s5, s6
	s_mul_hi_u32 s5, s6, s5
	s_add_i32 s6, s6, s5
	s_mul_hi_u32 s5, s1, s6
	s_mul_i32 s6, s5, s0
	s_sub_i32 s1, s1, s6
	s_add_i32 s7, s5, 1
	s_sub_i32 s6, s1, s0
	s_cmp_ge_u32 s1, s0
	s_cselect_b32 s5, s7, s5
	s_cselect_b32 s1, s6, s1
	s_add_i32 s6, s5, 1
	s_cmp_ge_u32 s1, s0
	s_cselect_b32 s0, s6, s5
	s_xor_b32 s0, s0, s4
	s_sub_i32 s6, s0, s4
	s_load_dwordx2 s[4:5], s[2:3], 0xd8
	s_load_dwordx2 s[0:1], s[2:3], 0x90
	s_min_i32 s2, s6, 0
	s_sub_i32 s2, 0, s2
	s_mul_i32 s3, s2, s87
	s_mul_hi_u32 s7, s2, s86
	s_add_i32 s7, s7, s3
	s_mul_i32 s2, s2, s86
	s_add_u32 s2, s2, s88
	s_addc_u32 s3, s7, s89
	v_cmp_lt_i64_e64 s[8:9], s[2:3], v[2:3]
	v_mov_b64_e32 v[2:3], 0x1ff
	v_cmp_gt_i64_e32 vcc, s[2:3], v[2:3]
	s_cbranch_vccnz .LBB0_887
	s_ashr_i32 s3, s2, 31
	s_lshr_b32 s3, s3, 29
	s_add_i32 s11, s2, s3
	s_and_b32 s3, s11, -8
	s_sub_i32 s7, s2, s3
	s_cmp_gt_i32 s7, -1
	s_cbranch_scc0 .LBB0_884
	s_lshl_b32 s10, s7, 6
	s_ashr_i32 s2, s11, 3
	s_cbranch_execz .LBB0_885
	s_branch .LBB0_886

; #define PG8_STAGE(bufoff, gbase, voff) do { _Pragma("unroll") for (int _i = 0; _i < 2; ++_i) \
;         __builtin_amdgcn_global_load_lds((const unsigned*)((const char*)(gbase) + (voff)[_i]), (PG8_LAS unsigned*)(lds + (bufoff) + ldsw + _i * 8192), 16, 0, 0); } while (0)
; #define PG8_LDA(dst, b, h) do { _Pragma("unroll") for (int m = 0; m < 4; ++m) _Pragma("unroll") for (int k = 0; k < 2; ++k) dst[m][k] = *(const PG8_LAS bf16x8*)(lds + PG8_SA(b, h) + aoff + m * 2048 + k * 1024); } while (0)
; #define PG8_LDB(dst, b, h) do { _Pragma("unroll") for (int n = 0; n < 2; ++n) _Pragma("unroll") for (int k = 0; k < 2; ++k) dst[n][k] = *(const PG8_LAS bf16x8*)(lds + PG8_SB(b, h) + boff + n * 2048 + k * 1024); } while (0)
; #define PG8_MMA(ai, bj, At, Bt) do { __builtin_amdgcn_s_setprio(1); _Pragma("unroll") for (int m = 0; m < 4; ++m) _Pragma("unroll") for (int n = 0; n < 2; ++n) _Pragma("unroll") for (int k = 0; k < 2; ++k) \
;         acc[ai][bj][m][n] = __builtin_amdgcn_mfma_f32_16x16x32_bf16(Bt[n][k], At[m][k], acc[ai][bj][m][n], 0, 0, 0); __builtin_amdgcn_s_setprio(0); } while (0)
; #define PG8_WAIT_V(n) asm volatile("s_waitcnt vmcnt(" #n ")" ::: "memory")
; #define PG8_WAIT_L(n) asm volatile("s_waitcnt lgkmcnt(" #n ")" ::: "memory")
; #define PG8_BAR __builtin_amdgcn_s_barrier()
; #define PG8_SCHED __builtin_amdgcn_sched_barrier(0)
; #define PG8_STAGE(bufoff, gbase, voff) do { _Pragma("unroll") for (int _i = 0; _i < 2; ++_i) \
;         __builtin_amdgcn_global_load_lds((const unsigned*)((const char*)(gbase) + (voff)[_i]), (PG8_LAS unsigned*)(lds + (bufoff) + ldsw + _i * 8192), 16, 0, 0); } while (0)
; #define PG8_LDA(dst, b, h) do { _Pragma("unroll") for (int m = 0; m < 4; ++m) _Pragma("unroll") for (int k = 0; k < 2; ++k) dst[m][k] = *(const PG8_LAS bf16x8*)(lds + PG8_SA(b, h) + aoff + m * 2048 + k * 1024); } while (0)
; #define PG8_WAIT_V(n) asm volatile("s_waitcnt vmcnt(" #n ")" ::: "memory")
; template <class Epi, class Sched, bool ALIGN_EPI = false, bool SP2 = false>
; __device__ __forceinline__ void gemm_phase(PG8_LAS unsigned char* lds, const Gemm g, const Sched& S, const Epi& E) {
;     ...
;             PG8_LDB(B0, 0, 0); PG8_LDB(B1, 0, 1); PG8_SCHED; PG8_LDA(At, 0, 0); PG8_STAGE(PG8_SA(1, 1), a1 + hstep, voffA);
;             PG8_WAIT_V(8); PG8_WAIT_L(0); PG8_BAR; PG8_MMA(0, 0, At, B0); PG8_MMA(0, 1, At, B1); PG8_BAR; PG8_SCHED;
.LBB0_900:
	ds_read_b128 v[114:117], v218
	ds_read_b128 v[118:121], v218 offset:1024
	ds_read_b128 v[138:141], v218 offset:2048
	ds_read_b128 v[142:145], v218 offset:3072
	ds_read_b128 v[146:149], v219
	ds_read_b128 v[150:153], v219 offset:1024
	ds_read_b128 v[154:157], v219 offset:2048
	ds_read_b128 v[158:161], v219 offset:3072
	s_add_u32 s34, s8, 0xfff80080
	s_addc_u32 s35, s9, -1
	s_cmp_eq_u32 s60, 28
	s_cselect_b32 s37, s19, s35
	s_cselect_b32 s36, s56, s34
	s_cselect_b32 s35, s17, s59
	s_cselect_b32 s34, s57, s58
	v_lshl_add_u64 v[170:171], s[8:9], 0, v[180:181]
	s_add_i32 m0, s27, 0xc000
	ds_read_b128 v[162:165], v220
	ds_read_b128 v[166:169], v220 offset:1024
	ds_read_b128 v[190:193], v220 offset:2048
	ds_read_b128 v[194:197], v220 offset:3072
	ds_read_b128 v[198:201], v220 offset:4096
	ds_read_b128 v[202:205], v220 offset:5120
	ds_read_b128 v[206:209], v220 offset:6144
	ds_read_b128 v[210:213], v220 offset:7168
	global_load_lds_dwordx4 v[170:171], off
	v_lshl_add_u64 v[170:171], s[8:9], 0, v[182:183]
	s_add_i32 m0, s27, 0xe000
	s_nop 0
	global_load_lds_dwordx4 v[170:171], off
	s_cmp_eq_u32 s100, 0
	s_cbranch_scc1 .Lllw6_a0
	s_waitcnt vmcnt(8)
.Lllw6_a0:
	s_waitcnt lgkmcnt(0)
	s_barrier
	s_setprio 1
	s_waitcnt lgkmcnt(0)
	v_mfma_f32_16x16x32_bf16 v[134:137], v[114:117], v[162:165], v[134:137]
	v_mfma_f32_16x16x32_bf16 v[130:133], v[138:141], v[162:165], v[130:133]
	v_mfma_f32_16x16x32_bf16 v[126:129], v[114:117], v[190:193], v[126:129]
	v_mfma_f32_16x16x32_bf16 v[122:125], v[138:141], v[190:193], v[122:125]
	v_mfma_f32_16x16x32_bf16 v[110:113], v[114:117], v[198:201], v[110:113]
	v_mfma_f32_16x16x32_bf16 v[106:109], v[138:141], v[198:201], v[106:109]
	v_mfma_f32_16x16x32_bf16 v[102:105], v[114:117], v[206:209], v[102:105]
	v_mfma_f32_16x16x32_bf16 v[98:101], v[138:141], v[206:209], v[98:101]
	v_mfma_f32_16x16x32_bf16 v[134:137], v[118:121], v[166:169], v[134:137]
	v_mfma_f32_16x16x32_bf16 v[130:133], v[142:145], v[166:169], v[130:133]
	v_mfma_f32_16x16x32_bf16 v[126:129], v[118:121], v[194:197], v[126:129]
	v_mfma_f32_16x16x32_bf16 v[122:125], v[142:145], v[194:197], v[122:125]
	v_mfma_f32_16x16x32_bf16 v[110:113], v[118:121], v[202:205], v[110:113]
	v_mfma_f32_16x16x32_bf16 v[106:109], v[142:145], v[202:205], v[106:109]
	v_mfma_f32_16x16x32_bf16 v[102:105], v[118:121], v[210:213], v[102:105]
	v_mfma_f32_16x16x32_bf16 v[98:101], v[142:145], v[210:213], v[98:101]
	s_setprio 0
	s_setprio 1
	v_mfma_f32_16x16x32_bf16 v[62:65], v[146:149], v[162:165], v[62:65]
	v_mfma_f32_16x16x32_bf16 v[58:61], v[154:157], v[162:165], v[58:61]
	v_mfma_f32_16x16x32_bf16 v[54:57], v[146:149], v[190:193], v[54:57]
	v_mfma_f32_16x16x32_bf16 v[50:53], v[154:157], v[190:193], v[50:53]
	v_mfma_f32_16x16x32_bf16 v[46:49], v[146:149], v[198:201], v[46:49]
	v_mfma_f32_16x16x32_bf16 v[42:45], v[154:157], v[198:201], v[42:45]
	v_mfma_f32_16x16x32_bf16 v[38:41], v[146:149], v[206:209], v[38:41]
	v_mfma_f32_16x16x32_bf16 v[34:37], v[154:157], v[206:209], v[34:37]
	v_mfma_f32_16x16x32_bf16 v[62:65], v[150:153], v[166:169], v[62:65]
	v_mfma_f32_16x16x32_bf16 v[58:61], v[158:161], v[166:169], v[58:61]
	v_mfma_f32_16x16x32_bf16 v[54:57], v[150:153], v[194:197], v[54:57]
	v_mfma_f32_16x16x32_bf16 v[50:53], v[158:161], v[194:197], v[50:53]
	v_mfma_f32_16x16x32_bf16 v[46:49], v[150:153], v[202:205], v[46:49]
	v_mfma_f32_16x16x32_bf16 v[42:45], v[158:161], v[202:205], v[42:45]
	v_mfma_f32_16x16x32_bf16 v[38:41], v[150:153], v[210:213], v[38:41]
	v_mfma_f32_16x16x32_bf16 v[34:37], v[158:161], v[210:213], v[34:37]
	s_setprio 0
	s_cmp_lg_u32 s100, 0
	s_cbranch_scc1 .Lllw6_b0
	s_waitcnt vmcnt(8)
; #define PG8_STAGE(bufoff, gbase, voff) do { _Pragma("unroll") for (int _i = 0; _i < 2; ++_i) \
;         __builtin_amdgcn_global_load_lds((const unsigned*)((const char*)(gbase) + (voff)[_i]), (PG8_LAS unsigned*)(lds + (bufoff) + ldsw + _i * 8192), 16, 0, 0); } while (0)
; #define PG8_LDA(dst, b, h) do { _Pragma("unroll") for (int m = 0; m < 4; ++m) _Pragma("unroll") for (int k = 0; k < 2; ++k) dst[m][k] = *(const PG8_LAS bf16x8*)(lds + PG8_SA(b, h) + aoff + m * 2048 + k * 1024); } while (0)
; #define PG8_LDB(dst, b, h) do { _Pragma("unroll") for (int n = 0; n < 2; ++n) _Pragma("unroll") for (int k = 0; k < 2; ++k) dst[n][k] = *(const PG8_LAS bf16x8*)(lds + PG8_SB(b, h) + boff + n * 2048 + k * 1024); } while (0)
; #define PG8_MMA(ai, bj, At, Bt) do { __builtin_amdgcn_s_setprio(1); _Pragma("unroll") for (int m = 0; m < 4; ++m) _Pragma("unroll") for (int n = 0; n < 2; ++n) _Pragma("unroll") for (int k = 0; k < 2; ++k) \
;         acc[ai][bj][m][n] = __builtin_amdgcn_mfma_f32_16x16x32_bf16(Bt[n][k], At[m][k], acc[ai][bj][m][n], 0, 0, 0); __builtin_amdgcn_s_setprio(0); } while (0)
; #define PG8_WAIT_V(n) asm volatile("s_waitcnt vmcnt(" #n ")" ::: "memory")
; #define PG8_WAIT_L(n) asm volatile("s_waitcnt lgkmcnt(" #n ")" ::: "memory")
; #define PG8_BAR __builtin_amdgcn_s_barrier()
; #define PG8_SCHED __builtin_amdgcn_sched_barrier(0)
; #define PG8_STAGE(bufoff, gbase, voff) do { _Pragma("unroll") for (int _i = 0; _i < 2; ++_i) \
;         __builtin_amdgcn_global_load_lds((const unsigned*)((const char*)(gbase) + (voff)[_i]), (PG8_LAS unsigned*)(lds + (bufoff) + ldsw + _i * 8192), 16, 0, 0); } while (0)
; #define PG8_BAR __builtin_amdgcn_s_barrier()
; template <class Epi, class Sched, bool ALIGN_EPI = false, bool SP2 = false>
; __device__ __forceinline__ void gemm_phase(PG8_LAS unsigned char* lds, const Gemm g, const Sched& S, const Epi& E) {
;     ...
;             PG8_WAIT_V(8); PG8_WAIT_L(0); PG8_BAR; PG8_MMA(0, 0, At, B0); PG8_MMA(0, 1, At, B1); PG8_BAR; PG8_SCHED;
;             PG8_LDA(At, 0, 1); PG8_STAGE(PG8_SB(0, 0), b2, voffB); PG8_STAGE(PG8_SB(0, 1), b2 + hstep, voffB); PG8_STAGE(PG8_SA(0, 0), a2, voffA);
;             PG8_WAIT_V(8); PG8_WAIT_L(0); PG8_BAR; PG8_MMA(1, 0, At, B0); PG8_MMA(1, 1, At, B1); PG8_BAR; PG8_SCHED;
;             PG8_LDB(B0, 1, 0); PG8_LDB(B1, 1, 1); PG8_SCHED; PG8_LDA(At, 1, 0); PG8_STAGE(PG8_SA(0, 1), a2 + hstep, voffA);
.Lllw6_b0:
	s_barrier
	s_add_i32 s61, s54, s40
	v_lshl_add_u64 v[170:171], s[34:35], 0, v[174:175]
	s_mov_b32 m0, s61
	ds_read_b128 v[162:165], v220 offset:16384
	ds_read_b128 v[166:169], v220 offset:17408
	ds_read_b128 v[190:193], v220 offset:18432
	ds_read_b128 v[194:197], v220 offset:19456
	ds_read_b128 v[198:201], v220 offset:20480
	ds_read_b128 v[202:205], v220 offset:21504
	ds_read_b128 v[206:209], v220 offset:22528
	ds_read_b128 v[210:213], v220 offset:23552
	global_load_lds_dwordx4 v[170:171], off
	s_add_i32 m0, s61, 0x2000
	s_add_u32 s62, s34, 0x80000
	v_lshl_add_u64 v[214:215], s[34:35], 0, v[178:179]
	s_addc_u32 s63, s35, 0
	s_add_i32 s61, s55, s40
	global_load_lds_dwordx4 v[214:215], off
	v_lshl_add_u64 v[222:223], s[62:63], 0, v[174:175]
	s_mov_b32 m0, s61
	v_lshl_add_u64 v[224:225], s[36:37], 0, v[176:177]
	global_load_lds_dwordx4 v[222:223], off
	v_lshl_add_u64 v[222:223], s[62:63], 0, v[178:179]
	s_add_i32 m0, s61, 0x2000
	s_nop 0
	global_load_lds_dwordx4 v[222:223], off
	v_lshl_add_u64 v[222:223], s[36:37], 0, v[172:173]
	s_mov_b32 m0, s27
	s_nop 0
	global_load_lds_dwordx4 v[222:223], off
	s_mov_b32 m0, s29
	s_nop 0
	global_load_lds_dwordx4 v[224:225], off
	s_cmp_eq_u32 s100, 0
	s_cbranch_scc1 .Lllw6_a1
	s_waitcnt vmcnt(8)
.Lllw6_a1:
	s_waitcnt lgkmcnt(0)
	s_barrier
	s_setprio 1
	s_waitcnt lgkmcnt(0)
	v_mfma_f32_16x16x32_bf16 v[94:97], v[114:117], v[162:165], v[94:97]
	v_mfma_f32_16x16x32_bf16 v[90:93], v[138:141], v[162:165], v[90:93]
	v_mfma_f32_16x16x32_bf16 v[86:89], v[114:117], v[190:193], v[86:89]
	v_mfma_f32_16x16x32_bf16 v[82:85], v[138:141], v[190:193], v[82:85]
	v_mfma_f32_16x16x32_bf16 v[78:81], v[114:117], v[198:201], v[78:81]
	v_mfma_f32_16x16x32_bf16 v[74:77], v[138:141], v[198:201], v[74:77]
	v_mfma_f32_16x16x32_bf16 v[70:73], v[114:117], v[206:209], v[70:73]
	v_mfma_f32_16x16x32_bf16 v[66:69], v[138:141], v[206:209], v[66:69]
	v_mfma_f32_16x16x32_bf16 v[94:97], v[118:121], v[166:169], v[94:97]
	v_mfma_f32_16x16x32_bf16 v[90:93], v[142:145], v[166:169], v[90:93]
	v_mfma_f32_16x16x32_bf16 v[86:89], v[118:121], v[194:197], v[86:89]
	v_mfma_f32_16x16x32_bf16 v[82:85], v[142:145], v[194:197], v[82:85]
	v_mfma_f32_16x16x32_bf16 v[78:81], v[118:121], v[202:205], v[78:81]
	v_mfma_f32_16x16x32_bf16 v[74:77], v[142:145], v[202:205], v[74:77]
	v_mfma_f32_16x16x32_bf16 v[70:73], v[118:121], v[210:213], v[70:73]
	v_mfma_f32_16x16x32_bf16 v[66:69], v[142:145], v[210:213], v[66:69]
	s_setprio 0
	s_setprio 1
	v_mfma_f32_16x16x32_bf16 v[30:33], v[146:149], v[162:165], v[30:33]
	v_mfma_f32_16x16x32_bf16 v[26:29], v[154:157], v[162:165], v[26:29]
	v_mfma_f32_16x16x32_bf16 v[22:25], v[146:149], v[190:193], v[22:25]
	v_mfma_f32_16x16x32_bf16 v[18:21], v[154:157], v[190:193], v[18:21]
	v_mfma_f32_16x16x32_bf16 v[14:17], v[146:149], v[198:201], v[14:17]
	v_mfma_f32_16x16x32_bf16 v[10:13], v[154:157], v[198:201], v[10:13]
	v_mfma_f32_16x16x32_bf16 v[6:9], v[146:149], v[206:209], v[6:9]
	v_mfma_f32_16x16x32_bf16 v[2:5], v[154:157], v[206:209], v[2:5]
	v_mfma_f32_16x16x32_bf16 v[30:33], v[150:153], v[166:169], v[30:33]
	v_mfma_f32_16x16x32_bf16 v[26:29], v[158:161], v[166:169], v[26:29]
	v_mfma_f32_16x16x32_bf16 v[22:25], v[150:153], v[194:197], v[22:25]
	v_mfma_f32_16x16x32_bf16 v[18:21], v[158:161], v[194:197], v[18:21]
	v_mfma_f32_16x16x32_bf16 v[14:17], v[150:153], v[202:205], v[14:17]
	v_mfma_f32_16x16x32_bf16 v[10:13], v[158:161], v[202:205], v[10:13]
	v_mfma_f32_16x16x32_bf16 v[6:9], v[150:153], v[210:213], v[6:9]
	v_mfma_f32_16x16x32_bf16 v[2:5], v[158:161], v[210:213], v[2:5]
	s_setprio 0
	s_cmp_lg_u32 s100, 0
	s_cbranch_scc1 .Lllw6_b1
	s_waitcnt vmcnt(8)
.Lllw6_b1:
	s_barrier
	s_add_i32 s61, 0, 0x18000
	s_add_i32 s62, 0, 0x1c000
	v_add_u32_e32 v142, s61, v217
	v_add_u32_e32 v158, s62, v217
	ds_read_b128 v[114:117], v142
	ds_read_b128 v[118:121], v142 offset:1024
	ds_read_b128 v[138:141], v142 offset:2048
	ds_read_b128 v[142:145], v142 offset:3072
	ds_read_b128 v[146:149], v158
	ds_read_b128 v[150:153], v158 offset:1024
	ds_read_b128 v[154:157], v158 offset:2048
	ds_read_b128 v[158:161], v158 offset:3072
	s_add_u32 s36, s36, 0x80000
	s_addc_u32 s37, s37, 0
	s_mov_b32 m0, s41
	v_lshl_add_u64 v[226:227], s[36:37], 0, v[172:173]
	ds_read_b128 v[162:165], v220 offset:32768
	ds_read_b128 v[166:169], v220 offset:33792
	ds_read_b128 v[190:193], v220 offset:34816
	ds_read_b128 v[194:197], v220 offset:35840
	ds_read_b128 v[198:201], v220 offset:36864
	ds_read_b128 v[202:205], v220 offset:37888
	ds_read_b128 v[206:209], v220 offset:38912
	ds_read_b128 v[210:213], v220 offset:39936
	global_load_lds_dwordx4 v[226:227], off
	v_lshl_add_u64 v[226:227], s[36:37], 0, v[176:177]
	s_mov_b32 m0, s42
	s_nop 0
	global_load_lds_dwordx4 v[226:227], off
	s_cmp_eq_u32 s100, 0
	s_cbranch_scc1 .Lllw6_a2
	s_waitcnt vmcnt(8)

; #define PG8_STAGE(bufoff, gbase, voff) do { _Pragma("unroll") for (int _i = 0; _i < 2; ++_i) \
;         __builtin_amdgcn_global_load_lds((const unsigned*)((const char*)(gbase) + (voff)[_i]), (PG8_LAS unsigned*)(lds + (bufoff) + ldsw + _i * 8192), 16, 0, 0); } while (0)
; #define PG8_LDA(dst, b, h) do { _Pragma("unroll") for (int m = 0; m < 4; ++m) _Pragma("unroll") for (int k = 0; k < 2; ++k) dst[m][k] = *(const PG8_LAS bf16x8*)(lds + PG8_SA(b, h) + aoff + m * 2048 + k * 1024); } while (0)
; #define PG8_MMA(ai, bj, At, Bt) do { __builtin_amdgcn_s_setprio(1); _Pragma("unroll") for (int m = 0; m < 4; ++m) _Pragma("unroll") for (int n = 0; n < 2; ++n) _Pragma("unroll") for (int k = 0; k < 2; ++k) \
;         acc[ai][bj][m][n] = __builtin_amdgcn_mfma_f32_16x16x32_bf16(Bt[n][k], At[m][k], acc[ai][bj][m][n], 0, 0, 0); __builtin_amdgcn_s_setprio(0); } while (0)
; #define PG8_WAIT_V(n) asm volatile("s_waitcnt vmcnt(" #n ")" ::: "memory")
; #define PG8_WAIT_L(n) asm volatile("s_waitcnt lgkmcnt(" #n ")" ::: "memory")
; #define PG8_BAR __builtin_amdgcn_s_barrier()
; #define PG8_SCHED __builtin_amdgcn_sched_barrier(0)
; #define PG8_STAGE(bufoff, gbase, voff) do { _Pragma("unroll") for (int _i = 0; _i < 2; ++_i) \
;         __builtin_amdgcn_global_load_lds((const unsigned*)((const char*)(gbase) + (voff)[_i]), (PG8_LAS unsigned*)(lds + (bufoff) + ldsw + _i * 8192), 16, 0, 0); } while (0)
; #define PG8_LDA(dst, b, h) do { _Pragma("unroll") for (int m = 0; m < 4; ++m) _Pragma("unroll") for (int k = 0; k < 2; ++k) dst[m][k] = *(const PG8_LAS bf16x8*)(lds + PG8_SA(b, h) + aoff + m * 2048 + k * 1024); } while (0)
; #define PG8_WAIT_V(n) asm volatile("s_waitcnt vmcnt(" #n ")" ::: "memory")
; #define PG8_WAIT_L(n) asm volatile("s_waitcnt lgkmcnt(" #n ")" ::: "memory")
; #define PG8_BAR __builtin_amdgcn_s_barrier()
; #define PG8_SCHED __builtin_amdgcn_sched_barrier(0)
; template <class Epi, class Sched, bool ALIGN_EPI = false, bool SP2 = false>
; __device__ __forceinline__ void gemm_phase(PG8_LAS unsigned char* lds, const Gemm g, const Sched& S, const Epi& E) {
;     ...
;             PG8_LDA(At, 1, 1); PG8_STAGE(PG8_SB(1, 0), b3, voffB); PG8_STAGE(PG8_SB(1, 1), b3 + hstep, voffB); PG8_STAGE(PG8_SA(1, 0), a3, voffA);
;             PG8_WAIT_V(8); PG8_WAIT_L(0); PG8_BAR; PG8_MMA(1, 0, At, B0); PG8_MMA(1, 1, At, B1); PG8_BAR; PG8_SCHED;
.Lllw6_b2:
	s_barrier
	s_add_i32 s36, s61, s40
	v_lshl_add_u64 v[170:171], v[170:171], 0, s[10:11]
	s_mov_b32 m0, s36
	ds_read_b128 v[162:165], v220 offset:49152
	ds_read_b128 v[166:169], v220 offset:50176
	ds_read_b128 v[190:193], v220 offset:51200
	ds_read_b128 v[194:197], v220 offset:52224
	ds_read_b128 v[198:201], v220 offset:53248
	ds_read_b128 v[202:205], v220 offset:54272
	ds_read_b128 v[206:209], v220 offset:55296
	ds_read_b128 v[210:213], v220 offset:56320
	global_load_lds_dwordx4 v[170:171], off
	s_add_i32 m0, s36, 0x2000
	s_add_u32 s34, s34, 0x80080
	v_lshl_add_u64 v[170:171], v[214:215], 0, s[10:11]
	s_addc_u32 s35, s35, 0
	s_add_i32 s36, s62, s40
	global_load_lds_dwordx4 v[170:171], off
	v_lshl_add_u64 v[170:171], s[34:35], 0, v[174:175]
	s_mov_b32 m0, s36
	s_nop 0
	global_load_lds_dwordx4 v[170:171], off
	v_lshl_add_u64 v[170:171], s[34:35], 0, v[178:179]
	s_add_i32 m0, s36, 0x2000
	s_nop 0
	global_load_lds_dwordx4 v[170:171], off
	v_lshl_add_u64 v[170:171], v[222:223], 0, s[10:11]
	s_mov_b32 m0, s51
	s_nop 0
	global_load_lds_dwordx4 v[170:171], off
	v_lshl_add_u64 v[170:171], v[224:225], 0, s[10:11]
	s_mov_b32 m0, s52
	s_nop 0
	global_load_lds_dwordx4 v[170:171], off
	s_cmp_eq_u32 s100, 0
	s_cbranch_scc1 .Lllw6_a3
	s_waitcnt vmcnt(8)

; #define PG8_MMA(ai, bj, At, Bt) do { __builtin_amdgcn_s_setprio(1); _Pragma("unroll") for (int m = 0; m < 4; ++m) _Pragma("unroll") for (int n = 0; n < 2; ++n) _Pragma("unroll") for (int k = 0; k < 2; ++k) \
;         acc[ai][bj][m][n] = __builtin_amdgcn_mfma_f32_16x16x32_bf16(Bt[n][k], At[m][k], acc[ai][bj][m][n], 0, 0, 0); __builtin_amdgcn_s_setprio(0); } while (0)
; #define PG8_WAIT_V(n) asm volatile("s_waitcnt vmcnt(" #n ")" ::: "memory")
; #define PG8_WAIT_L(n) asm volatile("s_waitcnt lgkmcnt(" #n ")" ::: "memory")
; #define PG8_BAR __builtin_amdgcn_s_barrier()
; #define PG8_SCHED __builtin_amdgcn_sched_barrier(0)
; #define PG8_MMA(ai, bj, At, Bt) do { __builtin_amdgcn_s_setprio(1); _Pragma("unroll") for (int m = 0; m < 4; ++m) _Pragma("unroll") for (int n = 0; n < 2; ++n) _Pragma("unroll") for (int k = 0; k < 2; ++k) \
;         acc[ai][bj][m][n] = __builtin_amdgcn_mfma_f32_16x16x32_bf16(Bt[n][k], At[m][k], acc[ai][bj][m][n], 0, 0, 0); __builtin_amdgcn_s_setprio(0); } while (0)
; #define PG8_WAIT_V(n) asm volatile("s_waitcnt vmcnt(" #n ")" ::: "memory")
; #define PG8_WAIT_L(n) asm volatile("s_waitcnt lgkmcnt(" #n ")" ::: "memory")
; #define PG8_BAR __builtin_amdgcn_s_barrier()
; #define PG8_SCHED __builtin_amdgcn_sched_barrier(0)
; template <class Epi, class Sched, bool ALIGN_EPI = false, bool SP2 = false>
; __device__ __forceinline__ void gemm_phase(PG8_LAS unsigned char* lds, const Gemm g, const Sched& S, const Epi& E) {
;     ...
;             PG8_WAIT_V(8); PG8_WAIT_L(0); PG8_BAR; PG8_MMA(1, 0, At, B0); PG8_MMA(1, 1, At, B1); PG8_BAR; PG8_SCHED;
;             } else {
.Lllw6_b3:
	s_barrier
	s_add_i32 s60, s60, 2
	s_add_u32 s8, s8, 0x100
	s_addc_u32 s9, s9, 0
	s_add_u32 s58, s58, 0x100
	s_addc_u32 s59, s59, 0
	s_cmp_gt_u32 s60, 29
	s_cbranch_scc0 .LBB0_900
	s_and_b64 vcc, exec, s[12:13]
	s_cbranch_vccz .LBB0_903
	s_barrier

;     __device__ __forceinline__ void init(int G_, int c_) { G = G_; c = c_; so.init(M, NPROJ, G_, c_); }
;     __device__ __forceinline__ bool next(int i, pg8::Unit& u) const { const int s = i >= R ? 1 : 0; const bool ok = so.next(i - s * R, u); u.sel = s; return ok && i < 2 * R; }
; #define PHASE_BASES() const KAS char* KA = (const KAS char*)__builtin_amdgcn_kernarg_segment_ptr(); asm volatile("" : "+s"(KA)); unsigned char* const ws = *(unsigned char* const KAS*)(KA + 8 * 27)
;     __host__ __device__ __forceinline__ bool next(int i, Unit& u) const {
;         const long L = (long)i * G + c; if (L >= nwg) return false;
;         int wgid = (int)L; { const int q = nwg / NXCD, r = nwg % NXCD, xcd = wgid % NXCD, off = wgid / NXCD; wgid = (xcd < r ? xcd * (q + 1) : r * (q + 1) + (xcd - r) * q) + off; }
;         const int nig = WGM * nN, gid = wgid / nig, fm = gid * WGM, gsz = (nM - fm) < WGM ? (nM - fm) : WGM;
;         u.pm = fm + ((wgid % nig) % gsz); u.pn = (wgid % nig) / gsz; return true;
; __global__ void __launch_bounds__(NWAVES * 64, 2) mk_fwd(Args args) {
;     ...
;     if (IN(7)) { PHASE_BASES();
;         pg8::Gemm g{MERGED, WO, M, D, D}; pg8::StaticOrder S; S.init(M, D, G, bx); EpiBf16Plain E{OUTX, D};
;         pg8::gemm_phase<EpiBf16Plain, pg8::StaticOrder, true, true>(lds, g, S, E);
.LBB0_993:
	v_readfirstlane_b32 s100, v0
	s_lshr_b32 s100, s100, 8
	s_cmp_lt_i32 s78, 8
	s_waitcnt lgkmcnt(0)
	s_cselect_b64 s[0:1], -1, 0
	s_cmp_gt_i32 s79, 7
	s_cselect_b64 s[2:3], -1, 0
	s_and_b64 s[0:1], s[0:1], s[2:3]
	s_andn2_b64 vcc, exec, s[0:1]
	s_cbranch_vccnz .LBB0_1072
	s_mov_b64 s[0:1], s[74:75]
	s_cmpk_gt_i32 s88, 0x1ff
	v_readfirstlane_b32 s9, v0
	s_cbranch_scc1 .LBB0_1018
	s_load_dwordx2 s[4:5], s[0:1], 0xd8
	s_lshr_b32 s0, s89, 29
	s_add_i32 s3, s88, s0
	s_and_b32 s0, s3, -8
	s_sub_i32 s6, s88, s0
	s_cmp_gt_i32 s6, -1
	s_cbranch_scc0 .LBB0_997
	s_lshl_b32 s2, s6, 6
	s_cbranch_execz .LBB0_998
	s_branch .LBB0_999

; #define PG8_STAGE(bufoff, gbase, voff) do { _Pragma("unroll") for (int _i = 0; _i < 2; ++_i) \
;         __builtin_amdgcn_global_load_lds((const unsigned*)((const char*)(gbase) + (voff)[_i]), (PG8_LAS unsigned*)(lds + (bufoff) + ldsw + _i * 8192), 16, 0, 0); } while (0)
; #define PG8_LDA(dst, b, h) do { _Pragma("unroll") for (int m = 0; m < 4; ++m) _Pragma("unroll") for (int k = 0; k < 2; ++k) dst[m][k] = *(const PG8_LAS bf16x8*)(lds + PG8_SA(b, h) + aoff + m * 2048 + k * 1024); } while (0)
; #define PG8_LDB(dst, b, h) do { _Pragma("unroll") for (int n = 0; n < 2; ++n) _Pragma("unroll") for (int k = 0; k < 2; ++k) dst[n][k] = *(const PG8_LAS bf16x8*)(lds + PG8_SB(b, h) + boff + n * 2048 + k * 1024); } while (0)
; #define PG8_MMA(ai, bj, At, Bt) do { __builtin_amdgcn_s_setprio(1); _Pragma("unroll") for (int m = 0; m < 4; ++m) _Pragma("unroll") for (int n = 0; n < 2; ++n) _Pragma("unroll") for (int k = 0; k < 2; ++k) \
;         acc[ai][bj][m][n] = __builtin_amdgcn_mfma_f32_16x16x32_bf16(Bt[n][k], At[m][k], acc[ai][bj][m][n], 0, 0, 0); __builtin_amdgcn_s_setprio(0); } while (0)
; #define PG8_WAIT_V(n) asm volatile("s_waitcnt vmcnt(" #n ")" ::: "memory")
; #define PG8_WAIT_L(n) asm volatile("s_waitcnt lgkmcnt(" #n ")" ::: "memory")
; #define PG8_BAR __builtin_amdgcn_s_barrier()
; #define PG8_SCHED __builtin_amdgcn_sched_barrier(0)
; #define PG8_STAGE(bufoff, gbase, voff) do { _Pragma("unroll") for (int _i = 0; _i < 2; ++_i) \
;         __builtin_amdgcn_global_load_lds((const unsigned*)((const char*)(gbase) + (voff)[_i]), (PG8_LAS unsigned*)(lds + (bufoff) + ldsw + _i * 8192), 16, 0, 0); } while (0)
; #define PG8_LDA(dst, b, h) do { _Pragma("unroll") for (int m = 0; m < 4; ++m) _Pragma("unroll") for (int k = 0; k < 2; ++k) dst[m][k] = *(const PG8_LAS bf16x8*)(lds + PG8_SA(b, h) + aoff + m * 2048 + k * 1024); } while (0)
; #define PG8_WAIT_V(n) asm volatile("s_waitcnt vmcnt(" #n ")" ::: "memory")
; template <class Epi, class Sched, bool ALIGN_EPI = false, bool SP2 = false>
; __device__ __forceinline__ void gemm_phase(PG8_LAS unsigned char* lds, const Gemm g, const Sched& S, const Epi& E) {
;     ...
;             PG8_LDB(B0, 0, 0); PG8_LDB(B1, 0, 1); PG8_SCHED; PG8_LDA(At, 0, 0); PG8_STAGE(PG8_SA(1, 1), a1 + hstep, voffA);
;             PG8_WAIT_V(8); PG8_WAIT_L(0); PG8_BAR; PG8_MMA(0, 0, At, B0); PG8_MMA(0, 1, At, B1); PG8_BAR; PG8_SCHED;
.LBB0_1011:
	ds_read_b128 v[154:157], v150
	ds_read_b128 v[158:161], v150 offset:1024
	ds_read_b128 v[162:165], v150 offset:2048
	ds_read_b128 v[166:169], v150 offset:3072
	ds_read_b128 v[170:173], v151
	ds_read_b128 v[174:177], v151 offset:1024
	ds_read_b128 v[178:181], v151 offset:2048
	ds_read_b128 v[182:185], v151 offset:3072
	s_add_u32 s34, s30, 0xfff80080
	s_addc_u32 s35, s31, -1
	s_cmp_eq_u32 s57, 28
	s_cselect_b32 s37, s23, s35
	s_cselect_b32 s36, s53, s34
	s_cselect_b32 s35, s21, s56
	s_cselect_b32 s34, s54, s55
	v_lshl_add_u64 v[146:147], s[30:31], 0, v[138:139]
	s_add_i32 m0, s29, 0xc000
	ds_read_b128 v[188:191], v152
	ds_read_b128 v[192:195], v152 offset:1024
	ds_read_b128 v[196:199], v152 offset:2048
	ds_read_b128 v[200:203], v152 offset:3072
	ds_read_b128 v[204:207], v152 offset:4096
	ds_read_b128 v[208:211], v152 offset:5120
	ds_read_b128 v[212:215], v152 offset:6144
	ds_read_b128 v[216:219], v152 offset:7168
	global_load_lds_dwordx4 v[146:147], off
	v_lshl_add_u64 v[146:147], s[30:31], 0, v[140:141]
	s_add_i32 m0, s29, 0xe000
	s_nop 0
	global_load_lds_dwordx4 v[146:147], off
	s_cmp_eq_u32 s100, 0
	s_cbranch_scc1 .Lllw7_a0
	s_waitcnt vmcnt(8)
.Lllw7_a0:
	s_waitcnt lgkmcnt(0)
	s_barrier
	s_setprio 1
	s_waitcnt lgkmcnt(0)
	v_mfma_f32_16x16x32_bf16 v[126:129], v[154:157], v[188:191], v[126:129]
	v_mfma_f32_16x16x32_bf16 v[122:125], v[162:165], v[188:191], v[122:125]
	v_mfma_f32_16x16x32_bf16 v[118:121], v[154:157], v[196:199], v[118:121]
	v_mfma_f32_16x16x32_bf16 v[110:113], v[162:165], v[196:199], v[110:113]
	v_mfma_f32_16x16x32_bf16 v[102:105], v[154:157], v[204:207], v[102:105]
	v_mfma_f32_16x16x32_bf16 v[94:97], v[162:165], v[204:207], v[94:97]
	v_mfma_f32_16x16x32_bf16 v[86:89], v[154:157], v[212:215], v[86:89]
	v_mfma_f32_16x16x32_bf16 v[78:81], v[162:165], v[212:215], v[78:81]
	v_mfma_f32_16x16x32_bf16 v[126:129], v[158:161], v[192:195], v[126:129]
	v_mfma_f32_16x16x32_bf16 v[122:125], v[166:169], v[192:195], v[122:125]
	v_mfma_f32_16x16x32_bf16 v[118:121], v[158:161], v[200:203], v[118:121]
	v_mfma_f32_16x16x32_bf16 v[110:113], v[166:169], v[200:203], v[110:113]
	v_mfma_f32_16x16x32_bf16 v[102:105], v[158:161], v[208:211], v[102:105]
	v_mfma_f32_16x16x32_bf16 v[94:97], v[166:169], v[208:211], v[94:97]
	v_mfma_f32_16x16x32_bf16 v[86:89], v[158:161], v[216:219], v[86:89]
	v_mfma_f32_16x16x32_bf16 v[78:81], v[166:169], v[216:219], v[78:81]
	s_setprio 0
	s_setprio 1
	v_mfma_f32_16x16x32_bf16 v[114:117], v[170:173], v[188:191], v[114:117]
	v_mfma_f32_16x16x32_bf16 v[106:109], v[178:181], v[188:191], v[106:109]
	v_mfma_f32_16x16x32_bf16 v[98:101], v[170:173], v[196:199], v[98:101]
	v_mfma_f32_16x16x32_bf16 v[90:93], v[178:181], v[196:199], v[90:93]
	v_mfma_f32_16x16x32_bf16 v[82:85], v[170:173], v[204:207], v[82:85]
	v_mfma_f32_16x16x32_bf16 v[74:77], v[178:181], v[204:207], v[74:77]
	v_mfma_f32_16x16x32_bf16 v[70:73], v[170:173], v[212:215], v[70:73]
	v_mfma_f32_16x16x32_bf16 v[66:69], v[178:181], v[212:215], v[66:69]
	v_mfma_f32_16x16x32_bf16 v[114:117], v[174:177], v[192:195], v[114:117]
	v_mfma_f32_16x16x32_bf16 v[106:109], v[182:185], v[192:195], v[106:109]
	v_mfma_f32_16x16x32_bf16 v[98:101], v[174:177], v[200:203], v[98:101]
	v_mfma_f32_16x16x32_bf16 v[90:93], v[182:185], v[200:203], v[90:93]
	v_mfma_f32_16x16x32_bf16 v[82:85], v[174:177], v[208:211], v[82:85]
	v_mfma_f32_16x16x32_bf16 v[74:77], v[182:185], v[208:211], v[74:77]
	v_mfma_f32_16x16x32_bf16 v[70:73], v[174:177], v[216:219], v[70:73]
	v_mfma_f32_16x16x32_bf16 v[66:69], v[182:185], v[216:219], v[66:69]
	s_setprio 0
	s_cmp_lg_u32 s100, 0
	s_cbranch_scc1 .Lllw7_b0
	s_waitcnt vmcnt(8)
; #define PG8_STAGE(bufoff, gbase, voff) do { _Pragma("unroll") for (int _i = 0; _i < 2; ++_i) \
;         __builtin_amdgcn_global_load_lds((const unsigned*)((const char*)(gbase) + (voff)[_i]), (PG8_LAS unsigned*)(lds + (bufoff) + ldsw + _i * 8192), 16, 0, 0); } while (0)
; #define PG8_LDA(dst, b, h) do { _Pragma("unroll") for (int m = 0; m < 4; ++m) _Pragma("unroll") for (int k = 0; k < 2; ++k) dst[m][k] = *(const PG8_LAS bf16x8*)(lds + PG8_SA(b, h) + aoff + m * 2048 + k * 1024); } while (0)
; #define PG8_LDB(dst, b, h) do { _Pragma("unroll") for (int n = 0; n < 2; ++n) _Pragma("unroll") for (int k = 0; k < 2; ++k) dst[n][k] = *(const PG8_LAS bf16x8*)(lds + PG8_SB(b, h) + boff + n * 2048 + k * 1024); } while (0)
; #define PG8_MMA(ai, bj, At, Bt) do { __builtin_amdgcn_s_setprio(1); _Pragma("unroll") for (int m = 0; m < 4; ++m) _Pragma("unroll") for (int n = 0; n < 2; ++n) _Pragma("unroll") for (int k = 0; k < 2; ++k) \
;         acc[ai][bj][m][n] = __builtin_amdgcn_mfma_f32_16x16x32_bf16(Bt[n][k], At[m][k], acc[ai][bj][m][n], 0, 0, 0); __builtin_amdgcn_s_setprio(0); } while (0)
; #define PG8_WAIT_V(n) asm volatile("s_waitcnt vmcnt(" #n ")" ::: "memory")
; #define PG8_WAIT_L(n) asm volatile("s_waitcnt lgkmcnt(" #n ")" ::: "memory")
; #define PG8_BAR __builtin_amdgcn_s_barrier()
; #define PG8_SCHED __builtin_amdgcn_sched_barrier(0)
; #define PG8_STAGE(bufoff, gbase, voff) do { _Pragma("unroll") for (int _i = 0; _i < 2; ++_i) \
;         __builtin_amdgcn_global_load_lds((const unsigned*)((const char*)(gbase) + (voff)[_i]), (PG8_LAS unsigned*)(lds + (bufoff) + ldsw + _i * 8192), 16, 0, 0); } while (0)
; #define PG8_BAR __builtin_amdgcn_s_barrier()
; template <class Epi, class Sched, bool ALIGN_EPI = false, bool SP2 = false>
; __device__ __forceinline__ void gemm_phase(PG8_LAS unsigned char* lds, const Gemm g, const Sched& S, const Epi& E) {
;     ...
;             PG8_WAIT_V(8); PG8_WAIT_L(0); PG8_BAR; PG8_MMA(0, 0, At, B0); PG8_MMA(0, 1, At, B1); PG8_BAR; PG8_SCHED;
;             PG8_LDA(At, 0, 1); PG8_STAGE(PG8_SB(0, 0), b2, voffB); PG8_STAGE(PG8_SB(0, 1), b2 + hstep, voffB); PG8_STAGE(PG8_SA(0, 0), a2, voffA);
;             PG8_WAIT_V(8); PG8_WAIT_L(0); PG8_BAR; PG8_MMA(1, 0, At, B0); PG8_MMA(1, 1, At, B1); PG8_BAR; PG8_SCHED;
;             PG8_LDB(B0, 1, 0); PG8_LDB(B1, 1, 1); PG8_SCHED; PG8_LDA(At, 1, 0); PG8_STAGE(PG8_SA(0, 1), a2 + hstep, voffA);
.Lllw7_b0:
	s_barrier
	s_add_i32 s58, s46, s39
	v_lshl_add_u64 v[146:147], s[34:35], 0, v[132:133]
	s_mov_b32 m0, s58
	ds_read_b128 v[188:191], v152 offset:16384
	ds_read_b128 v[192:195], v152 offset:17408
	ds_read_b128 v[196:199], v152 offset:18432
	ds_read_b128 v[200:203], v152 offset:19456
	ds_read_b128 v[204:207], v152 offset:20480
	ds_read_b128 v[208:211], v152 offset:21504
	ds_read_b128 v[212:215], v152 offset:22528
	ds_read_b128 v[216:219], v152 offset:23552
	global_load_lds_dwordx4 v[146:147], off
	s_add_i32 m0, s58, 0x2000
	s_add_u32 s58, s34, 0x80000
	v_lshl_add_u64 v[220:221], s[34:35], 0, v[136:137]
	s_addc_u32 s59, s35, 0
	s_add_i32 s60, s47, s39
	global_load_lds_dwordx4 v[220:221], off
	v_lshl_add_u64 v[222:223], s[58:59], 0, v[132:133]
	s_mov_b32 m0, s60
	v_lshl_add_u64 v[224:225], s[36:37], 0, v[134:135]
	global_load_lds_dwordx4 v[222:223], off
	v_lshl_add_u64 v[222:223], s[58:59], 0, v[136:137]
	s_add_i32 m0, s60, 0x2000
	s_nop 0
	global_load_lds_dwordx4 v[222:223], off
	v_lshl_add_u64 v[222:223], s[36:37], 0, v[130:131]
	s_mov_b32 m0, s29
	s_nop 0
	global_load_lds_dwordx4 v[222:223], off
	s_mov_b32 m0, s40
	s_nop 0
	global_load_lds_dwordx4 v[224:225], off
	s_cmp_eq_u32 s100, 0
	s_cbranch_scc1 .Lllw7_a1
	s_waitcnt vmcnt(8)
.Lllw7_a1:
	s_waitcnt lgkmcnt(0)
	s_barrier
	s_setprio 1
	s_waitcnt lgkmcnt(0)
	v_mfma_f32_16x16x32_bf16 v[62:65], v[154:157], v[188:191], v[62:65]
	v_mfma_f32_16x16x32_bf16 v[58:61], v[162:165], v[188:191], v[58:61]
	v_mfma_f32_16x16x32_bf16 v[54:57], v[154:157], v[196:199], v[54:57]
	v_mfma_f32_16x16x32_bf16 v[46:49], v[162:165], v[196:199], v[46:49]
	v_mfma_f32_16x16x32_bf16 v[38:41], v[154:157], v[204:207], v[38:41]
	v_mfma_f32_16x16x32_bf16 v[30:33], v[162:165], v[204:207], v[30:33]
	v_mfma_f32_16x16x32_bf16 v[22:25], v[154:157], v[212:215], v[22:25]
	v_mfma_f32_16x16x32_bf16 v[14:17], v[162:165], v[212:215], v[14:17]
	v_mfma_f32_16x16x32_bf16 v[62:65], v[158:161], v[192:195], v[62:65]
	v_mfma_f32_16x16x32_bf16 v[58:61], v[166:169], v[192:195], v[58:61]
	v_mfma_f32_16x16x32_bf16 v[54:57], v[158:161], v[200:203], v[54:57]
	v_mfma_f32_16x16x32_bf16 v[46:49], v[166:169], v[200:203], v[46:49]
	v_mfma_f32_16x16x32_bf16 v[38:41], v[158:161], v[208:211], v[38:41]
	v_mfma_f32_16x16x32_bf16 v[30:33], v[166:169], v[208:211], v[30:33]
	v_mfma_f32_16x16x32_bf16 v[22:25], v[158:161], v[216:219], v[22:25]
	v_mfma_f32_16x16x32_bf16 v[14:17], v[166:169], v[216:219], v[14:17]
	s_setprio 0
	s_setprio 1
	v_mfma_f32_16x16x32_bf16 v[50:53], v[170:173], v[188:191], v[50:53]
	v_mfma_f32_16x16x32_bf16 v[42:45], v[178:181], v[188:191], v[42:45]
	v_mfma_f32_16x16x32_bf16 v[34:37], v[170:173], v[196:199], v[34:37]
	v_mfma_f32_16x16x32_bf16 v[26:29], v[178:181], v[196:199], v[26:29]
	v_mfma_f32_16x16x32_bf16 v[18:21], v[170:173], v[204:207], v[18:21]
	v_mfma_f32_16x16x32_bf16 v[10:13], v[178:181], v[204:207], v[10:13]
	v_mfma_f32_16x16x32_bf16 v[6:9], v[170:173], v[212:215], v[6:9]
	v_mfma_f32_16x16x32_bf16 v[2:5], v[178:181], v[212:215], v[2:5]
	v_mfma_f32_16x16x32_bf16 v[50:53], v[174:177], v[192:195], v[50:53]
	v_mfma_f32_16x16x32_bf16 v[42:45], v[182:185], v[192:195], v[42:45]
	v_mfma_f32_16x16x32_bf16 v[34:37], v[174:177], v[200:203], v[34:37]
	v_mfma_f32_16x16x32_bf16 v[26:29], v[182:185], v[200:203], v[26:29]
	v_mfma_f32_16x16x32_bf16 v[18:21], v[174:177], v[208:211], v[18:21]
	v_mfma_f32_16x16x32_bf16 v[10:13], v[182:185], v[208:211], v[10:13]
	v_mfma_f32_16x16x32_bf16 v[6:9], v[174:177], v[216:219], v[6:9]
	v_mfma_f32_16x16x32_bf16 v[2:5], v[182:185], v[216:219], v[2:5]
	s_setprio 0
	s_cmp_lg_u32 s100, 0
	s_cbranch_scc1 .Lllw7_b1
	s_waitcnt vmcnt(8)
.Lllw7_b1:
	s_barrier
	s_add_i32 s58, 0, 0x18000
	v_add_u32_e32 v153, s58, v148
	s_add_i32 s59, 0, 0x1c000
	ds_read_b128 v[154:157], v153
	ds_read_b128 v[158:161], v153 offset:1024
	ds_read_b128 v[162:165], v153 offset:2048
	ds_read_b128 v[166:169], v153 offset:3072
	v_add_u32_e32 v153, s59, v148
	ds_read_b128 v[170:173], v153
	ds_read_b128 v[174:177], v153 offset:1024
	ds_read_b128 v[178:181], v153 offset:2048
	ds_read_b128 v[182:185], v153 offset:3072
	s_add_u32 s36, s36, 0x80000
	s_addc_u32 s37, s37, 0
	s_mov_b32 m0, s41
	v_lshl_add_u64 v[226:227], s[36:37], 0, v[130:131]
	ds_read_b128 v[188:191], v152 offset:32768
	ds_read_b128 v[192:195], v152 offset:33792
	ds_read_b128 v[196:199], v152 offset:34816
	ds_read_b128 v[200:203], v152 offset:35840
	ds_read_b128 v[204:207], v152 offset:36864
	ds_read_b128 v[208:211], v152 offset:37888
	ds_read_b128 v[212:215], v152 offset:38912
	ds_read_b128 v[216:219], v152 offset:39936
	global_load_lds_dwordx4 v[226:227], off
	v_lshl_add_u64 v[226:227], s[36:37], 0, v[134:135]
	s_mov_b32 m0, s42
	s_nop 0
	global_load_lds_dwordx4 v[226:227], off
	s_cmp_eq_u32 s100, 0
	s_cbranch_scc1 .Lllw7_a2
	s_waitcnt vmcnt(8)

; #define PG8_STAGE(bufoff, gbase, voff) do { _Pragma("unroll") for (int _i = 0; _i < 2; ++_i) \
;         __builtin_amdgcn_global_load_lds((const unsigned*)((const char*)(gbase) + (voff)[_i]), (PG8_LAS unsigned*)(lds + (bufoff) + ldsw + _i * 8192), 16, 0, 0); } while (0)
; #define PG8_LDA(dst, b, h) do { _Pragma("unroll") for (int m = 0; m < 4; ++m) _Pragma("unroll") for (int k = 0; k < 2; ++k) dst[m][k] = *(const PG8_LAS bf16x8*)(lds + PG8_SA(b, h) + aoff + m * 2048 + k * 1024); } while (0)
; #define PG8_MMA(ai, bj, At, Bt) do { __builtin_amdgcn_s_setprio(1); _Pragma("unroll") for (int m = 0; m < 4; ++m) _Pragma("unroll") for (int n = 0; n < 2; ++n) _Pragma("unroll") for (int k = 0; k < 2; ++k) \
;         acc[ai][bj][m][n] = __builtin_amdgcn_mfma_f32_16x16x32_bf16(Bt[n][k], At[m][k], acc[ai][bj][m][n], 0, 0, 0); __builtin_amdgcn_s_setprio(0); } while (0)
; #define PG8_WAIT_V(n) asm volatile("s_waitcnt vmcnt(" #n ")" ::: "memory")
; #define PG8_WAIT_L(n) asm volatile("s_waitcnt lgkmcnt(" #n ")" ::: "memory")
; #define PG8_BAR __builtin_amdgcn_s_barrier()
; #define PG8_SCHED __builtin_amdgcn_sched_barrier(0)
; #define PG8_STAGE(bufoff, gbase, voff) do { _Pragma("unroll") for (int _i = 0; _i < 2; ++_i) \
;         __builtin_amdgcn_global_load_lds((const unsigned*)((const char*)(gbase) + (voff)[_i]), (PG8_LAS unsigned*)(lds + (bufoff) + ldsw + _i * 8192), 16, 0, 0); } while (0)
; #define PG8_LDA(dst, b, h) do { _Pragma("unroll") for (int m = 0; m < 4; ++m) _Pragma("unroll") for (int k = 0; k < 2; ++k) dst[m][k] = *(const PG8_LAS bf16x8*)(lds + PG8_SA(b, h) + aoff + m * 2048 + k * 1024); } while (0)
; #define PG8_WAIT_V(n) asm volatile("s_waitcnt vmcnt(" #n ")" ::: "memory")
; #define PG8_WAIT_L(n) asm volatile("s_waitcnt lgkmcnt(" #n ")" ::: "memory")
; #define PG8_BAR __builtin_amdgcn_s_barrier()
; #define PG8_SCHED __builtin_amdgcn_sched_barrier(0)
; template <class Epi, class Sched, bool ALIGN_EPI = false, bool SP2 = false>
; __device__ __forceinline__ void gemm_phase(PG8_LAS unsigned char* lds, const Gemm g, const Sched& S, const Epi& E) {
;     ...
;             PG8_LDA(At, 1, 1); PG8_STAGE(PG8_SB(1, 0), b3, voffB); PG8_STAGE(PG8_SB(1, 1), b3 + hstep, voffB); PG8_STAGE(PG8_SA(1, 0), a3, voffA);
;             PG8_WAIT_V(8); PG8_WAIT_L(0); PG8_BAR; PG8_MMA(1, 0, At, B0); PG8_MMA(1, 1, At, B1); PG8_BAR; PG8_SCHED;
.Lllw7_b2:
	s_barrier
	s_add_i32 s36, s58, s39
	v_lshl_add_u64 v[146:147], v[146:147], 0, s[10:11]
	s_mov_b32 m0, s36
	ds_read_b128 v[188:191], v152 offset:49152
	ds_read_b128 v[192:195], v152 offset:50176
	ds_read_b128 v[196:199], v152 offset:51200
	ds_read_b128 v[200:203], v152 offset:52224
	ds_read_b128 v[204:207], v152 offset:53248
	ds_read_b128 v[208:211], v152 offset:54272
	ds_read_b128 v[212:215], v152 offset:55296
	ds_read_b128 v[216:219], v152 offset:56320
	global_load_lds_dwordx4 v[146:147], off
	s_add_i32 m0, s36, 0x2000
	s_add_u32 s34, s34, 0x80080
	v_lshl_add_u64 v[146:147], v[220:221], 0, s[10:11]
	s_addc_u32 s35, s35, 0
	s_add_i32 s36, s59, s39
	global_load_lds_dwordx4 v[146:147], off
	v_lshl_add_u64 v[146:147], s[34:35], 0, v[132:133]
	s_mov_b32 m0, s36
	s_nop 0
	global_load_lds_dwordx4 v[146:147], off
	v_lshl_add_u64 v[146:147], s[34:35], 0, v[136:137]
	s_add_i32 m0, s36, 0x2000
	s_nop 0
	global_load_lds_dwordx4 v[146:147], off
	v_lshl_add_u64 v[146:147], v[222:223], 0, s[10:11]
	s_mov_b32 m0, s44
	s_nop 0
	global_load_lds_dwordx4 v[146:147], off
	v_lshl_add_u64 v[146:147], v[224:225], 0, s[10:11]
	s_mov_b32 m0, s45
	s_nop 0
	global_load_lds_dwordx4 v[146:147], off
	s_cmp_eq_u32 s100, 0
	s_cbranch_scc1 .Lllw7_a3
	s_waitcnt vmcnt(8)

; #define PG8_MMA(ai, bj, At, Bt) do { __builtin_amdgcn_s_setprio(1); _Pragma("unroll") for (int m = 0; m < 4; ++m) _Pragma("unroll") for (int n = 0; n < 2; ++n) _Pragma("unroll") for (int k = 0; k < 2; ++k) \
;         acc[ai][bj][m][n] = __builtin_amdgcn_mfma_f32_16x16x32_bf16(Bt[n][k], At[m][k], acc[ai][bj][m][n], 0, 0, 0); __builtin_amdgcn_s_setprio(0); } while (0)
; #define PG8_WAIT_V(n) asm volatile("s_waitcnt vmcnt(" #n ")" ::: "memory")
; #define PG8_WAIT_L(n) asm volatile("s_waitcnt lgkmcnt(" #n ")" ::: "memory")
; #define PG8_BAR __builtin_amdgcn_s_barrier()
; #define PG8_SCHED __builtin_amdgcn_sched_barrier(0)
; #define PG8_MMA(ai, bj, At, Bt) do { __builtin_amdgcn_s_setprio(1); _Pragma("unroll") for (int m = 0; m < 4; ++m) _Pragma("unroll") for (int n = 0; n < 2; ++n) _Pragma("unroll") for (int k = 0; k < 2; ++k) \
;         acc[ai][bj][m][n] = __builtin_amdgcn_mfma_f32_16x16x32_bf16(Bt[n][k], At[m][k], acc[ai][bj][m][n], 0, 0, 0); __builtin_amdgcn_s_setprio(0); } while (0)
; #define PG8_WAIT_V(n) asm volatile("s_waitcnt vmcnt(" #n ")" ::: "memory")
; #define PG8_WAIT_L(n) asm volatile("s_waitcnt lgkmcnt(" #n ")" ::: "memory")
; #define PG8_BAR __builtin_amdgcn_s_barrier()
; #define PG8_SCHED __builtin_amdgcn_sched_barrier(0)
; template <class Epi, class Sched, bool ALIGN_EPI = false, bool SP2 = false>
; __device__ __forceinline__ void gemm_phase(PG8_LAS unsigned char* lds, const Gemm g, const Sched& S, const Epi& E) {
;     ...
;             PG8_WAIT_V(8); PG8_WAIT_L(0); PG8_BAR; PG8_MMA(1, 0, At, B0); PG8_MMA(1, 1, At, B1); PG8_BAR; PG8_SCHED;
;             } else {
.Lllw7_b3:
	s_barrier
	s_add_i32 s57, s57, 2
	s_add_u32 s30, s30, 0x100
	s_addc_u32 s31, s31, 0
	s_add_u32 s55, s55, 0x100
	s_addc_u32 s56, s56, 0
	s_cmp_gt_u32 s57, 29
	s_cbranch_scc0 .LBB0_1011
	s_and_b64 vcc, exec, s[12:13]
	s_cbranch_vccz .LBB0_1014
	s_barrier

; #define LAS __attribute__((address_space(3)))
;     __device__ __forceinline__ void init(int G_, int c_) { G = G_; c = c_; so.init(M, NPROJ, G_, c_); }
;     __device__ __forceinline__ bool next(int i, pg8::Unit& u) const { const int s = i >= R ? 1 : 0; const bool ok = so.next(i - s * R, u); u.sel = s; return ok && i < 2 * R; }
; #define PHASE_BASES() const KAS char* KA = (const KAS char*)__builtin_amdgcn_kernarg_segment_ptr(); asm volatile("" : "+s"(KA)); unsigned char* const ws = *(unsigned char* const KAS*)(KA + 8 * 27)
; template <class Epi, class Sched>
; __device__ __forceinline__ void gemm_phase_gather(PG8_LAS unsigned char* lds, const Gemm g, const int* __restrict__ gidx, PG8_LAS int* itab  , const Sched& S, const Epi& E) {
;     ...
;     { int vals[4];
; #pragma unroll
;       for (int k = 0; k < 4; ++k) { const int e = tid + 512 * k; Unit uu; const bool ok = S.next(e >> 8, uu); vals[k] = ok ? gidx[uu.pm * BM + (e & 255)] : 0; }
; __global__ void __launch_bounds__(NWAVES * 64, 2) mk_fwd(Args args) {
;     ...
;     if (IN(10)) { PHASE_BASES();
;         pg8::Gemm g{HX2, W13, NB * NE * CAP, NE * 2 * FF, D}; OrderMoe<16> S; S.init(G, bx); EpiMoe1 E{ACT};
;         pg8::gemm_phase_gather<EpiMoe1, OrderMoe<16>>(lds, g, IDX, (LAS int*)(lds + 131072), S, E);
.LBB0_1258:
	v_readfirstlane_b32 s100, v0
	s_lshr_b32 s100, s100, 8
	s_cmp_lt_i32 s78, 11
	s_cselect_b64 s[0:1], -1, 0
	s_cmp_gt_i32 s79, 10
	s_cselect_b64 s[2:3], -1, 0
	s_and_b64 s[0:1], s[0:1], s[2:3]
	s_andn2_b64 vcc, exec, s[0:1]
	s_cbranch_vccnz .LBB0_1339
	s_mov_b64 s[0:1], s[74:75]
	s_load_dwordx2 s[0:1], s[0:1], 0xd8
	v_lshrrev_b32_e32 v2, 8, v0
	v_mul_lo_u32 v2, s86, v2
	v_add_u32_e32 v4, s88, v2
	s_movk_i32 s7, 0x800
	s_waitcnt lgkmcnt(0)
	s_add_u32 s2, s0, 0x400000
	v_readfirstlane_b32 s6, v0
	v_and_b32_e32 v1, 0xff, v0
	s_addc_u32 s3, s1, 0
	v_cmp_gt_i32_e32 vcc, s7, v4
	v_mov_b32_e32 v2, 0
	v_mov_b32_e32 v3, 0
	s_and_saveexec_b64 s[4:5], vcc
	s_cbranch_execz .LBB0_1261
	v_ashrrev_i32_e32 v3, 31, v4
	v_lshrrev_b32_e32 v3, 29, v3
	v_add_u32_e32 v3, v4, v3
	v_ashrrev_i32_e32 v5, 3, v3
	v_and_b32_e32 v3, 0xfffff8, v3
	v_sub_u32_e32 v3, v4, v3
	v_lshl_add_u32 v3, v3, 8, v5
	v_ashrrev_i32_e32 v5, 31, v3
	v_lshrrev_b32_e32 v5, 25, v5
	v_add_u32_e32 v5, v3, v5
	v_lshrrev_b32_e32 v6, 7, v5
	v_and_b32_e32 v5, 0xff80, v5
	v_sub_u32_e32 v3, v3, v5
	v_mov_b32_e32 v5, 12
	v_lshrrev_b16_sdwa v5, v5, sext(v3) dst_sel:DWORD dst_unused:UNUSED_PAD src0_sel:DWORD src1_sel:BYTE_0
	v_and_b32_e32 v5, 7, v5
	v_add_u16_e32 v5, v3, v5
	v_and_b32_e32 v5, 0xf8, v5
	v_sub_u16_e32 v3, v3, v5
	v_mov_b32_e32 v5, 3
	v_lshlrev_b32_sdwa v5, v5, sext(v3) dst_sel:DWORD dst_unused:UNUSED_PAD src0_sel:DWORD src1_sel:BYTE_0
	v_and_b32_e32 v5, 0x7ffff0, v5
	v_lshlrev_b32_e32 v3, 8, v3
	v_add_lshl_u32 v5, v5, v6, 9
	v_and_b32_e32 v3, 0x100, v3
	v_or3_b32 v6, v5, v3, v1
	v_ashrrev_i32_e32 v7, 31, v6
	v_lshl_add_u64 v[6:7], v[6:7], 2, s[2:3]
	global_load_dword v3, v[6:7], off

; #define PG8_STAGE(bufoff, gbase, voff) do { _Pragma("unroll") for (int _i = 0; _i < 2; ++_i) \
;         __builtin_amdgcn_global_load_lds((const unsigned*)((const char*)(gbase) + (voff)[_i]), (PG8_LAS unsigned*)(lds + (bufoff) + ldsw + _i * 8192), 16, 0, 0); } while (0)
; #define PG8_LDA(dst, b, h) do { _Pragma("unroll") for (int m = 0; m < 4; ++m) _Pragma("unroll") for (int k = 0; k < 2; ++k) dst[m][k] = *(const PG8_LAS bf16x8*)(lds + PG8_SA(b, h) + aoff + m * 2048 + k * 1024); } while (0)
; #define PG8_LDB(dst, b, h) do { _Pragma("unroll") for (int n = 0; n < 2; ++n) _Pragma("unroll") for (int k = 0; k < 2; ++k) dst[n][k] = *(const PG8_LAS bf16x8*)(lds + PG8_SB(b, h) + boff + n * 2048 + k * 1024); } while (0)
; #define PG8_MMA(ai, bj, At, Bt) do { __builtin_amdgcn_s_setprio(1); _Pragma("unroll") for (int m = 0; m < 4; ++m) _Pragma("unroll") for (int n = 0; n < 2; ++n) _Pragma("unroll") for (int k = 0; k < 2; ++k) \
;         acc[ai][bj][m][n] = __builtin_amdgcn_mfma_f32_16x16x32_bf16(Bt[n][k], At[m][k], acc[ai][bj][m][n], 0, 0, 0); __builtin_amdgcn_s_setprio(0); } while (0)
; #define PG8_WAIT_V(n) asm volatile("s_waitcnt vmcnt(" #n ")" ::: "memory")
; #define PG8_WAIT_L(n) asm volatile("s_waitcnt lgkmcnt(" #n ")" ::: "memory")
; #define PG8_BAR __builtin_amdgcn_s_barrier()
; #define PG8_SCHED __builtin_amdgcn_sched_barrier(0)
; template <class Epi, class Sched>
; __device__ __forceinline__ void gemm_phase_gather(PG8_LAS unsigned char* lds, const Gemm g, const int* __restrict__ gidx, PG8_LAS int* itab  , const Sched& S, const Epi& E) {
;     ...
;             const bool last = (t == nt - 2);
;             const char* a1 = gA + (size_t)(t + 1) * kstep;
;             const char* a2 = last ? gA : gA + (size_t)(t + 2) * kstep; const char* b2 = last ? nB : cB + (size_t)(t + 2) * kstep;
;             const char* a3 = a2 + kstep; const char* b3 = b2 + kstep;
;             unsigned vo2[2][2];
; #pragma unroll
;             for (int _h = 0; _h < 2; ++_h)
; #pragma unroll
;                 for (int _i = 0; _i < 2; ++_i) vo2[_h][_i] = last ? nvo[_h][_i] : cvo[_h][_i];
;             if (last && has_next) S.a_ready(nxt);
;             PG8_LDB(B0, 0, 0); PG8_LDB(B1, 0, 1); PG8_SCHED; PG8_LDA(At, 0, 0); PG8_STAGE(PG8_SA(1, 1), a1, cvo[1]);
;             PG8_WAIT_V(8); PG8_WAIT_L(0); PG8_BAR; PG8_MMA(0, 0, At, B0); PG8_MMA(0, 1, At, B1); PG8_BAR; PG8_SCHED;
.LBB0_1278:
	ds_read_b128 v[158:161], v150
	ds_read_b128 v[162:165], v150 offset:1024
	ds_read_b128 v[166:169], v150 offset:2048
	ds_read_b128 v[170:173], v150 offset:3072
	ds_read_b128 v[174:177], v151
	ds_read_b128 v[178:181], v151 offset:1024
	ds_read_b128 v[182:185], v151 offset:2048
	ds_read_b128 v[188:191], v151 offset:3072
	s_add_u32 s24, s0, s22
	s_addc_u32 s25, s1, s23
	s_add_u32 s26, s24, 0xe800100
	s_addc_u32 s27, s25, 0
	s_add_u32 s50, s47, s22
	s_addc_u32 s51, s48, s23
	s_cmpk_eq_i32 s22, 0xf00
	s_cselect_b64 vcc, -1, 0
	s_and_b64 s[24:25], vcc, exec
	v_cndmask_b32_e32 v134, v157, v153, vcc
	s_cselect_b32 s27, s3, s27
	s_cselect_b32 s26, s2, s26
	v_cndmask_b32_e32 v224, v140, v154, vcc
	v_cndmask_b32_e32 v137, v138, v155, vcc
	v_cndmask_b32_e32 v139, v136, v156, vcc
	s_cselect_b32 s25, s17, s51
	s_cselect_b32 s24, s46, s50
	s_mov_b32 m0, s43
	v_lshl_add_u64 v[226:227], v[144:145], 0, s[22:23]
	ds_read_b128 v[192:195], v152
	ds_read_b128 v[196:199], v152 offset:1024
	ds_read_b128 v[200:203], v152 offset:2048
	ds_read_b128 v[204:207], v152 offset:3072
	ds_read_b128 v[208:211], v152 offset:4096
	ds_read_b128 v[212:215], v152 offset:5120
	ds_read_b128 v[216:219], v152 offset:6144
	ds_read_b128 v[220:223], v152 offset:7168
	global_load_lds_dwordx4 v[226:227], off
	v_lshl_add_u64 v[226:227], v[142:143], 0, s[22:23]
	s_add_i32 m0, s21, 0xe000
	s_nop 0
	global_load_lds_dwordx4 v[226:227], off
	s_cmp_eq_u32 s100, 0
	s_cbranch_scc1 .Lllw10_a0
	s_waitcnt vmcnt(8)
.Lllw10_a0:
	s_waitcnt lgkmcnt(0)
	s_barrier
	s_setprio 1
	s_waitcnt lgkmcnt(0)
	v_mfma_f32_16x16x32_bf16 v[126:129], v[158:161], v[192:195], v[126:129]
	v_mfma_f32_16x16x32_bf16 v[122:125], v[166:169], v[192:195], v[122:125]
	v_mfma_f32_16x16x32_bf16 v[110:113], v[158:161], v[200:203], v[110:113]
	v_mfma_f32_16x16x32_bf16 v[106:109], v[166:169], v[200:203], v[106:109]
	v_mfma_f32_16x16x32_bf16 v[94:97], v[158:161], v[208:211], v[94:97]
	v_mfma_f32_16x16x32_bf16 v[90:93], v[166:169], v[208:211], v[90:93]
	v_mfma_f32_16x16x32_bf16 v[78:81], v[158:161], v[216:219], v[78:81]
	v_mfma_f32_16x16x32_bf16 v[74:77], v[166:169], v[216:219], v[74:77]
	v_mfma_f32_16x16x32_bf16 v[126:129], v[162:165], v[196:199], v[126:129]
	v_mfma_f32_16x16x32_bf16 v[122:125], v[170:173], v[196:199], v[122:125]
	v_mfma_f32_16x16x32_bf16 v[110:113], v[162:165], v[204:207], v[110:113]
	v_mfma_f32_16x16x32_bf16 v[106:109], v[170:173], v[204:207], v[106:109]
	v_mfma_f32_16x16x32_bf16 v[94:97], v[162:165], v[212:215], v[94:97]
	v_mfma_f32_16x16x32_bf16 v[90:93], v[170:173], v[212:215], v[90:93]
	v_mfma_f32_16x16x32_bf16 v[78:81], v[162:165], v[220:223], v[78:81]
	v_mfma_f32_16x16x32_bf16 v[74:77], v[170:173], v[220:223], v[74:77]
	s_setprio 0
	s_setprio 1
	v_mfma_f32_16x16x32_bf16 v[118:121], v[174:177], v[192:195], v[118:121]
	v_mfma_f32_16x16x32_bf16 v[114:117], v[182:185], v[192:195], v[114:117]
	v_mfma_f32_16x16x32_bf16 v[102:105], v[174:177], v[200:203], v[102:105]
	v_mfma_f32_16x16x32_bf16 v[98:101], v[182:185], v[200:203], v[98:101]
	v_mfma_f32_16x16x32_bf16 v[86:89], v[174:177], v[208:211], v[86:89]
	v_mfma_f32_16x16x32_bf16 v[82:85], v[182:185], v[208:211], v[82:85]
	v_mfma_f32_16x16x32_bf16 v[70:73], v[174:177], v[216:219], v[70:73]
	v_mfma_f32_16x16x32_bf16 v[66:69], v[182:185], v[216:219], v[66:69]
	v_mfma_f32_16x16x32_bf16 v[118:121], v[178:181], v[196:199], v[118:121]
	v_mfma_f32_16x16x32_bf16 v[114:117], v[188:191], v[196:199], v[114:117]
	v_mfma_f32_16x16x32_bf16 v[102:105], v[178:181], v[204:207], v[102:105]
	v_mfma_f32_16x16x32_bf16 v[98:101], v[188:191], v[204:207], v[98:101]
	v_mfma_f32_16x16x32_bf16 v[86:89], v[178:181], v[212:215], v[86:89]
	v_mfma_f32_16x16x32_bf16 v[82:85], v[188:191], v[212:215], v[82:85]
	v_mfma_f32_16x16x32_bf16 v[70:73], v[178:181], v[220:223], v[70:73]
	v_mfma_f32_16x16x32_bf16 v[66:69], v[188:191], v[220:223], v[66:69]
	s_setprio 0
	s_cmp_lg_u32 s100, 0
	s_cbranch_scc1 .Lllw10_b0
	s_waitcnt vmcnt(8)
; #define PG8_STAGE(bufoff, gbase, voff) do { _Pragma("unroll") for (int _i = 0; _i < 2; ++_i) \
;         __builtin_amdgcn_global_load_lds((const unsigned*)((const char*)(gbase) + (voff)[_i]), (PG8_LAS unsigned*)(lds + (bufoff) + ldsw + _i * 8192), 16, 0, 0); } while (0)
; #define PG8_LDA(dst, b, h) do { _Pragma("unroll") for (int m = 0; m < 4; ++m) _Pragma("unroll") for (int k = 0; k < 2; ++k) dst[m][k] = *(const PG8_LAS bf16x8*)(lds + PG8_SA(b, h) + aoff + m * 2048 + k * 1024); } while (0)
; #define PG8_LDB(dst, b, h) do { _Pragma("unroll") for (int n = 0; n < 2; ++n) _Pragma("unroll") for (int k = 0; k < 2; ++k) dst[n][k] = *(const PG8_LAS bf16x8*)(lds + PG8_SB(b, h) + boff + n * 2048 + k * 1024); } while (0)
; #define PG8_MMA(ai, bj, At, Bt) do { __builtin_amdgcn_s_setprio(1); _Pragma("unroll") for (int m = 0; m < 4; ++m) _Pragma("unroll") for (int n = 0; n < 2; ++n) _Pragma("unroll") for (int k = 0; k < 2; ++k) \
;         acc[ai][bj][m][n] = __builtin_amdgcn_mfma_f32_16x16x32_bf16(Bt[n][k], At[m][k], acc[ai][bj][m][n], 0, 0, 0); __builtin_amdgcn_s_setprio(0); } while (0)
; #define PG8_WAIT_V(n) asm volatile("s_waitcnt vmcnt(" #n ")" ::: "memory")
; #define PG8_WAIT_L(n) asm volatile("s_waitcnt lgkmcnt(" #n ")" ::: "memory")
; #define PG8_BAR __builtin_amdgcn_s_barrier()
; #define PG8_SCHED __builtin_amdgcn_sched_barrier(0)
; #define PG8_STAGE(bufoff, gbase, voff) do { _Pragma("unroll") for (int _i = 0; _i < 2; ++_i) \
;         __builtin_amdgcn_global_load_lds((const unsigned*)((const char*)(gbase) + (voff)[_i]), (PG8_LAS unsigned*)(lds + (bufoff) + ldsw + _i * 8192), 16, 0, 0); } while (0)
; #define PG8_BAR __builtin_amdgcn_s_barrier()
; template <class Epi, class Sched>
; __device__ __forceinline__ void gemm_phase_gather(PG8_LAS unsigned char* lds, const Gemm g, const int* __restrict__ gidx, PG8_LAS int* itab  , const Sched& S, const Epi& E) {
;     ...
;             PG8_WAIT_V(8); PG8_WAIT_L(0); PG8_BAR; PG8_MMA(0, 0, At, B0); PG8_MMA(0, 1, At, B1); PG8_BAR; PG8_SCHED;
;             PG8_LDA(At, 0, 1); PG8_STAGE(PG8_SB(0, 0), b2, voffB); PG8_STAGE(PG8_SB(0, 1), b2 + hstep, voffB); PG8_STAGE(PG8_SA(0, 0), a2, vo2[0]);
;             PG8_WAIT_V(8); PG8_WAIT_L(0); PG8_BAR; PG8_MMA(1, 0, At, B0); PG8_MMA(1, 1, At, B1); PG8_BAR; PG8_SCHED;
;             PG8_LDB(B0, 1, 0); PG8_LDB(B1, 1, 1); PG8_SCHED; PG8_LDA(At, 1, 0); PG8_STAGE(PG8_SA(0, 1), a2, vo2[1]);
.Lllw10_b0:
	s_barrier
	s_add_i32 s50, s38, s28
	v_lshl_add_u64 v[226:227], s[24:25], 0, v[130:131]
	s_mov_b32 m0, s50
	ds_read_b128 v[192:195], v152 offset:16384
	ds_read_b128 v[196:199], v152 offset:17408
	ds_read_b128 v[200:203], v152 offset:18432
	ds_read_b128 v[204:207], v152 offset:19456
	ds_read_b128 v[208:211], v152 offset:20480
	ds_read_b128 v[212:215], v152 offset:21504
	ds_read_b128 v[216:219], v152 offset:22528
	ds_read_b128 v[220:223], v152 offset:23552
	global_load_lds_dwordx4 v[226:227], off
	s_add_i32 m0, s50, 0x2000
	s_add_u32 s50, s24, 0x80000
	v_lshl_add_u64 v[228:229], s[24:25], 0, v[132:133]
	s_addc_u32 s51, s25, 0
	s_add_i32 s52, s39, s28
	global_load_lds_dwordx4 v[228:229], off
	v_lshl_add_u64 v[230:231], s[50:51], 0, v[130:131]
	s_mov_b32 m0, s52
	v_mov_b32_e32 v225, v135
	global_load_lds_dwordx4 v[230:231], off
	v_lshl_add_u64 v[230:231], s[50:51], 0, v[132:133]
	s_add_i32 m0, s52, 0x2000
	s_nop 0
	global_load_lds_dwordx4 v[230:231], off
	s_mov_b32 m0, s21
	v_lshl_add_u64 v[230:231], s[26:27], 0, v[134:135]
	global_load_lds_dwordx4 v134, s[26:27]
	s_mov_b32 m0, s31
	s_nop 0
	global_load_lds_dwordx4 v224, s[26:27]
	s_cmp_eq_u32 s100, 0
	s_cbranch_scc1 .Lllw10_a1
	s_waitcnt vmcnt(8)
.Lllw10_a1:
	s_waitcnt lgkmcnt(0)
	v_lshl_add_u64 v[224:225], s[26:27], 0, v[224:225]
	s_barrier
	s_setprio 1
	s_waitcnt lgkmcnt(0)
	v_mfma_f32_16x16x32_bf16 v[62:65], v[158:161], v[192:195], v[62:65]
	v_mfma_f32_16x16x32_bf16 v[58:61], v[166:169], v[192:195], v[58:61]
	v_mfma_f32_16x16x32_bf16 v[46:49], v[158:161], v[200:203], v[46:49]
	v_mfma_f32_16x16x32_bf16 v[38:41], v[166:169], v[200:203], v[38:41]
	v_mfma_f32_16x16x32_bf16 v[14:17], v[158:161], v[208:211], v[14:17]
	v_mfma_f32_16x16x32_bf16 v[10:13], v[166:169], v[208:211], v[10:13]
	v_mfma_f32_16x16x32_bf16 v[6:9], v[158:161], v[216:219], v[6:9]
	v_mfma_f32_16x16x32_bf16 v[2:5], v[166:169], v[216:219], v[2:5]
	v_mfma_f32_16x16x32_bf16 v[62:65], v[162:165], v[196:199], v[62:65]
	v_mfma_f32_16x16x32_bf16 v[58:61], v[170:173], v[196:199], v[58:61]
	v_mfma_f32_16x16x32_bf16 v[46:49], v[162:165], v[204:207], v[46:49]
	v_mfma_f32_16x16x32_bf16 v[38:41], v[170:173], v[204:207], v[38:41]
	v_mfma_f32_16x16x32_bf16 v[14:17], v[162:165], v[212:215], v[14:17]
	v_mfma_f32_16x16x32_bf16 v[10:13], v[170:173], v[212:215], v[10:13]
	v_mfma_f32_16x16x32_bf16 v[6:9], v[162:165], v[220:223], v[6:9]
	v_mfma_f32_16x16x32_bf16 v[2:5], v[170:173], v[220:223], v[2:5]
	s_setprio 0
	s_setprio 1
	v_mfma_f32_16x16x32_bf16 v[54:57], v[174:177], v[192:195], v[54:57]
	v_mfma_f32_16x16x32_bf16 v[50:53], v[182:185], v[192:195], v[50:53]
	v_mfma_f32_16x16x32_bf16 v[30:33], v[174:177], v[200:203], v[30:33]
	v_mfma_f32_16x16x32_bf16 v[26:29], v[182:185], v[200:203], v[26:29]
	v_mfma_f32_16x16x32_bf16 v[42:45], v[174:177], v[208:211], v[42:45]
	v_mfma_f32_16x16x32_bf16 v[34:37], v[182:185], v[208:211], v[34:37]
	v_mfma_f32_16x16x32_bf16 v[22:25], v[174:177], v[216:219], v[22:25]
	v_mfma_f32_16x16x32_bf16 v[18:21], v[182:185], v[216:219], v[18:21]
	v_mfma_f32_16x16x32_bf16 v[54:57], v[178:181], v[196:199], v[54:57]
	v_mfma_f32_16x16x32_bf16 v[50:53], v[188:191], v[196:199], v[50:53]
	v_mfma_f32_16x16x32_bf16 v[30:33], v[178:181], v[204:207], v[30:33]
	v_mfma_f32_16x16x32_bf16 v[26:29], v[188:191], v[204:207], v[26:29]
	v_mfma_f32_16x16x32_bf16 v[42:45], v[178:181], v[212:215], v[42:45]
	v_mfma_f32_16x16x32_bf16 v[34:37], v[188:191], v[212:215], v[34:37]
	v_mfma_f32_16x16x32_bf16 v[22:25], v[178:181], v[220:223], v[22:25]
	v_mfma_f32_16x16x32_bf16 v[18:21], v[188:191], v[220:223], v[18:21]
	s_setprio 0
	s_cmp_lg_u32 s100, 0
	s_cbranch_scc1 .Lllw10_b1
	s_waitcnt vmcnt(8)
.Lllw10_b1:
	s_barrier
	s_add_i32 s50, 0, 0x18000
	v_add_u32_e32 v134, s50, v148
	s_add_i32 s51, 0, 0x1c000
	ds_read_b128 v[158:161], v134
	ds_read_b128 v[162:165], v134 offset:1024
	ds_read_b128 v[166:169], v134 offset:2048
	ds_read_b128 v[170:173], v134 offset:3072
	v_add_u32_e32 v134, s51, v148
	ds_read_b128 v[174:177], v134
	ds_read_b128 v[178:181], v134 offset:1024
	ds_read_b128 v[182:185], v134 offset:2048
	ds_read_b128 v[188:191], v134 offset:3072
	s_mov_b32 m0, s33
	ds_read_b128 v[192:195], v152 offset:32768
	ds_read_b128 v[196:199], v152 offset:33792
	ds_read_b128 v[200:203], v152 offset:34816
	ds_read_b128 v[204:207], v152 offset:35840
	ds_read_b128 v[208:211], v152 offset:36864
	ds_read_b128 v[212:215], v152 offset:37888
	ds_read_b128 v[216:219], v152 offset:38912
	ds_read_b128 v[220:223], v152 offset:39936
	global_load_lds_dwordx4 v137, s[26:27]
	s_mov_b32 m0, s34
	s_nop 0
	global_load_lds_dwordx4 v139, s[26:27]
	s_cmp_eq_u32 s100, 0
	s_cbranch_scc1 .Lllw10_a2
	s_waitcnt vmcnt(8)

; #define PG8_STAGE(bufoff, gbase, voff) do { _Pragma("unroll") for (int _i = 0; _i < 2; ++_i) \
;         __builtin_amdgcn_global_load_lds((const unsigned*)((const char*)(gbase) + (voff)[_i]), (PG8_LAS unsigned*)(lds + (bufoff) + ldsw + _i * 8192), 16, 0, 0); } while (0)
; #define PG8_LDA(dst, b, h) do { _Pragma("unroll") for (int m = 0; m < 4; ++m) _Pragma("unroll") for (int k = 0; k < 2; ++k) dst[m][k] = *(const PG8_LAS bf16x8*)(lds + PG8_SA(b, h) + aoff + m * 2048 + k * 1024); } while (0)
; #define PG8_MMA(ai, bj, At, Bt) do { __builtin_amdgcn_s_setprio(1); _Pragma("unroll") for (int m = 0; m < 4; ++m) _Pragma("unroll") for (int n = 0; n < 2; ++n) _Pragma("unroll") for (int k = 0; k < 2; ++k) \
;         acc[ai][bj][m][n] = __builtin_amdgcn_mfma_f32_16x16x32_bf16(Bt[n][k], At[m][k], acc[ai][bj][m][n], 0, 0, 0); __builtin_amdgcn_s_setprio(0); } while (0)
; #define PG8_WAIT_V(n) asm volatile("s_waitcnt vmcnt(" #n ")" ::: "memory")
; #define PG8_WAIT_L(n) asm volatile("s_waitcnt lgkmcnt(" #n ")" ::: "memory")
; #define PG8_BAR __builtin_amdgcn_s_barrier()
; #define PG8_SCHED __builtin_amdgcn_sched_barrier(0)
; #define PG8_STAGE(bufoff, gbase, voff) do { _Pragma("unroll") for (int _i = 0; _i < 2; ++_i) \
;         __builtin_amdgcn_global_load_lds((const unsigned*)((const char*)(gbase) + (voff)[_i]), (PG8_LAS unsigned*)(lds + (bufoff) + ldsw + _i * 8192), 16, 0, 0); } while (0)
; #define PG8_LDA(dst, b, h) do { _Pragma("unroll") for (int m = 0; m < 4; ++m) _Pragma("unroll") for (int k = 0; k < 2; ++k) dst[m][k] = *(const PG8_LAS bf16x8*)(lds + PG8_SA(b, h) + aoff + m * 2048 + k * 1024); } while (0)
; #define PG8_WAIT_V(n) asm volatile("s_waitcnt vmcnt(" #n ")" ::: "memory")
; #define PG8_WAIT_L(n) asm volatile("s_waitcnt lgkmcnt(" #n ")" ::: "memory")
; #define PG8_BAR __builtin_amdgcn_s_barrier()
; #define PG8_SCHED __builtin_amdgcn_sched_barrier(0)
; template <class Epi, class Sched>
; __device__ __forceinline__ void gemm_phase_gather(PG8_LAS unsigned char* lds, const Gemm g, const int* __restrict__ gidx, PG8_LAS int* itab  , const Sched& S, const Epi& E) {
;     ...
;             PG8_LDA(At, 1, 1); PG8_STAGE(PG8_SB(1, 0), b3, voffB); PG8_STAGE(PG8_SB(1, 1), b3 + hstep, voffB); PG8_STAGE(PG8_SA(1, 0), a3, vo2[0]);
;             PG8_WAIT_V(8); PG8_WAIT_L(0); PG8_BAR; PG8_MMA(1, 0, At, B0); PG8_MMA(1, 1, At, B1); PG8_BAR; PG8_SCHED;
;         }
.Lllw10_b2:
	s_barrier
	s_add_i32 s26, s50, s28
	v_lshl_add_u64 v[226:227], v[226:227], 0, s[10:11]
	s_mov_b32 m0, s26
	ds_read_b128 v[192:195], v152 offset:49152
	ds_read_b128 v[196:199], v152 offset:50176
	ds_read_b128 v[200:203], v152 offset:51200
	ds_read_b128 v[204:207], v152 offset:52224
	ds_read_b128 v[208:211], v152 offset:53248
	ds_read_b128 v[212:215], v152 offset:54272
	ds_read_b128 v[216:219], v152 offset:55296
	ds_read_b128 v[220:223], v152 offset:56320
	global_load_lds_dwordx4 v[226:227], off
	s_add_i32 m0, s26, 0x2000
	s_add_u32 s24, s24, 0x80080
	v_lshl_add_u64 v[226:227], v[228:229], 0, s[10:11]
	s_addc_u32 s25, s25, 0
	s_add_i32 s26, s51, s28
	global_load_lds_dwordx4 v[226:227], off
	v_lshl_add_u64 v[226:227], s[24:25], 0, v[130:131]
	s_mov_b32 m0, s26
	v_lshl_add_u64 v[224:225], v[224:225], 0, s[10:11]
	global_load_lds_dwordx4 v[226:227], off
	v_lshl_add_u64 v[226:227], s[24:25], 0, v[132:133]
	s_add_i32 m0, s26, 0x2000
	s_nop 0
	global_load_lds_dwordx4 v[226:227], off
	v_lshl_add_u64 v[226:227], v[230:231], 0, s[10:11]
	s_mov_b32 m0, s35
	s_nop 0
	global_load_lds_dwordx4 v[226:227], off
	s_mov_b32 m0, s36
	s_nop 0
	global_load_lds_dwordx4 v[224:225], off
	s_cmp_eq_u32 s100, 0
	s_cbranch_scc1 .Lllw10_a3
	s_waitcnt vmcnt(8)
.Lllw10_a3:
	s_waitcnt lgkmcnt(0)
	s_barrier
	s_setprio 1
	s_waitcnt lgkmcnt(0)
	v_mfma_f32_16x16x32_bf16 v[62:65], v[158:161], v[192:195], v[62:65]
	v_mfma_f32_16x16x32_bf16 v[58:61], v[166:169], v[192:195], v[58:61]
	v_mfma_f32_16x16x32_bf16 v[46:49], v[158:161], v[200:203], v[46:49]
	v_mfma_f32_16x16x32_bf16 v[38:41], v[166:169], v[200:203], v[38:41]
	v_mfma_f32_16x16x32_bf16 v[14:17], v[158:161], v[208:211], v[14:17]
	v_mfma_f32_16x16x32_bf16 v[10:13], v[166:169], v[208:211], v[10:13]
	v_mfma_f32_16x16x32_bf16 v[6:9], v[158:161], v[216:219], v[6:9]
	v_mfma_f32_16x16x32_bf16 v[2:5], v[166:169], v[216:219], v[2:5]
	v_mfma_f32_16x16x32_bf16 v[62:65], v[162:165], v[196:199], v[62:65]
	v_mfma_f32_16x16x32_bf16 v[58:61], v[170:173], v[196:199], v[58:61]
	v_mfma_f32_16x16x32_bf16 v[46:49], v[162:165], v[204:207], v[46:49]
	v_mfma_f32_16x16x32_bf16 v[38:41], v[170:173], v[204:207], v[38:41]
	v_mfma_f32_16x16x32_bf16 v[14:17], v[162:165], v[212:215], v[14:17]
	v_mfma_f32_16x16x32_bf16 v[10:13], v[170:173], v[212:215], v[10:13]
	v_mfma_f32_16x16x32_bf16 v[6:9], v[162:165], v[220:223], v[6:9]
	v_mfma_f32_16x16x32_bf16 v[2:5], v[170:173], v[220:223], v[2:5]
	s_setprio 0
	s_setprio 1
	v_mfma_f32_16x16x32_bf16 v[54:57], v[174:177], v[192:195], v[54:57]
	v_mfma_f32_16x16x32_bf16 v[50:53], v[182:185], v[192:195], v[50:53]
	v_mfma_f32_16x16x32_bf16 v[30:33], v[174:177], v[200:203], v[30:33]
	v_mfma_f32_16x16x32_bf16 v[26:29], v[182:185], v[200:203], v[26:29]
	v_mfma_f32_16x16x32_bf16 v[42:45], v[174:177], v[208:211], v[42:45]
	v_mfma_f32_16x16x32_bf16 v[34:37], v[182:185], v[208:211], v[34:37]
	v_mfma_f32_16x16x32_bf16 v[22:25], v[174:177], v[216:219], v[22:25]
	v_mfma_f32_16x16x32_bf16 v[18:21], v[182:185], v[216:219], v[18:21]
	v_mfma_f32_16x16x32_bf16 v[54:57], v[178:181], v[196:199], v[54:57]
	v_mfma_f32_16x16x32_bf16 v[50:53], v[188:191], v[196:199], v[50:53]
	v_mfma_f32_16x16x32_bf16 v[30:33], v[178:181], v[204:207], v[30:33]
	v_mfma_f32_16x16x32_bf16 v[26:29], v[188:191], v[204:207], v[26:29]
	v_mfma_f32_16x16x32_bf16 v[42:45], v[178:181], v[212:215], v[42:45]
	v_mfma_f32_16x16x32_bf16 v[34:37], v[188:191], v[212:215], v[34:37]
	v_mfma_f32_16x16x32_bf16 v[22:25], v[178:181], v[220:223], v[22:25]
	v_mfma_f32_16x16x32_bf16 v[18:21], v[188:191], v[220:223], v[18:21]
	s_setprio 0
	s_cmp_lg_u32 s100, 0
	s_cbranch_scc1 .Lllw10_b3
	s_waitcnt vmcnt(8)
.Lllw10_b3:
	s_barrier
	s_add_i32 s49, s49, 2
	s_add_u32 s22, s22, 0x100
	s_addc_u32 s23, s23, 0
	s_cmp_gt_u32 s49, 29
	s_cbranch_scc0 .LBB0_1278
	s_and_b64 vcc, exec, s[14:15]
	s_cbranch_vccz .LBB0_1281
	s_barrier

; #define PG8_STAGE(bufoff, gbase, voff) do { _Pragma("unroll") for (int _i = 0; _i < 2; ++_i) \
;         __builtin_amdgcn_global_load_lds((const unsigned*)((const char*)(gbase) + (voff)[_i]), (PG8_LAS unsigned*)(lds + (bufoff) + ldsw + _i * 8192), 16, 0, 0); } while (0)
; #define PG8_BAR __builtin_amdgcn_s_barrier()
; #define PG8_BAR __builtin_amdgcn_s_barrier()
; template <class Epi, class Sched, bool ALIGN_EPI = false, bool SP2 = false>
; __device__ __forceinline__ void gemm_phase(PG8_LAS unsigned char* lds, const Gemm g, const Sched& S, const Epi& E) {
;     ...
;     for (int i = 0; i < 2; ++i) { int R, C; stage_rc(tid * 16 + i * 8192, R, C); const int Rb = Epi::PERM ? ((R & ~31) + perm32(R & 31)) : R;
;         voffA[i] = (unsigned)(R * K + C) * 2u; voffB[i] = (unsigned)(Rb * K + C) * 2u; }
;     const size_t kstep = (size_t)(BK * 2);
;     const size_t hstep = (size_t)HALF * K * 2;
;     const size_t tstep = 2 * hstep;
;     const unsigned ldsw = (unsigned)wid * 1024u;
;     const int aoff = lds_byte(wr * 64 + fr, fq * 8), boff = lds_byte(wc * 32 + fr, fq * 8);
;     ...
;     Unit cur, nxt; int ui = 0;
;     if (!S.next(0, cur)) return;
;     f32x4 acc[2][2][4][2];
; #pragma unroll
;     for (int a = 0; a < 2; ++a)
; #pragma unroll
;         for (int b = 0; b < 2; ++b)
; #pragma unroll
;             for (int m = 0; m < 4; ++m)
; #pragma unroll
;                 for (int n = 0; n < 2; ++n) acc[a][b][m][n] = (f32x4){0.f, 0.f, 0.f, 0.f};
;     bf16x8 At[4][2], B0[2][2], B1[2][2];
;     const char* cA = (const char*)(cur.sel ? g.A2 : g.A) + (size_t)cur.pm * tstep; const char* cB = (const char*)(cur.sel ? g.Bt2 : g.Bt) + (size_t)cur.pn * tstep;
;     S.a_ready(cur);
;     if constexpr (SP2) {
;         PG8_STAGE(PG8_SB(0, 0), cB, voffB); PG8_STAGE(PG8_SB(0, 1), cB + hstep, voffB); PG8_STAGE(PG8_SA(0, 0), cA, voffA); PG8_STAGE(PG8_SA(0, 1), cA + hstep, voffA);
;         if (wr == 1) PG8_BAR;
;     __device__ __forceinline__ bool next(int i, pg8::Unit& u) const {
;         constexpr int NWG = NE * 8 * NJ, Q = NWG / 8;
;         const int L = i * G + c; if (L >= NWG) return false;
;         const int wgid = (L % 8) * Q + L / 8;
;         const int e = wgid / (8 * NJ), w = wgid % (8 * NJ), rt = w % 8, j = w / 8, b = rt >> 1, half = rt & 1;
;         u.pm = (b * NE + e) * 2 + half; u.pn = e * NJ + j; return true;
.LBB0_1339:
	v_readfirstlane_b32 s100, v0
	s_lshr_b32 s100, s100, 8
	s_cmp_lt_i32 s78, 12
	s_cselect_b64 s[0:1], -1, 0
	s_cmp_gt_i32 s79, 11
	s_cselect_b64 s[2:3], -1, 0
	s_and_b64 s[0:1], s[0:1], s[2:3]
	s_andn2_b64 vcc, exec, s[0:1]
	s_cbranch_vccnz .LBB0_1410
	s_mov_b64 s[0:1], s[74:75]
	s_cmpk_gt_i32 s88, 0x3ff
	v_readfirstlane_b32 s10, v0
	s_cbranch_scc1 .LBB0_1356
	s_load_dwordx2 s[6:7], s[0:1], 0xd8
	v_lshrrev_b32_e32 v1, 5, v0
	v_lshrrev_b32_e32 v3, 1, v0
	v_and_b32_e32 v1, 4, v1
	v_bfe_u32 v2, v0, 2, 2
	v_and_b32_e32 v12, 24, v3
	v_lshlrev_b32_e32 v3, 4, v0
	s_waitcnt lgkmcnt(0)
	s_add_u32 s33, s6, 0x2800000
	v_or3_b32 v2, v1, v2, v12
	v_or_b32_e32 v1, 0x2000, v3
	s_addc_u32 s40, s7, 0
	v_lshrrev_b32_e32 v4, 7, v1
	s_movk_i32 s0, 0x60
	s_add_u32 s41, s6, 0x39700000
	v_and_or_b32 v5, v4, s0, v2
	v_bfe_u32 v13, v0, 2, 4
	s_movk_i32 s0, 0x70
	s_addc_u32 s42, s7, 0
	v_and_or_b32 v4, v4, s0, v13
	s_lshr_b32 s0, s89, 29
	s_add_i32 s0, s88, s0
	s_ashr_i32 s0, s0, 3
	s_lshl_b32 s1, s88, 7
	s_mulk_i32 s0, 0xfc01
	s_add_i32 s0, s0, s1
	s_ashr_i32 s1, s0, 31
	s_lshr_b32 s1, s1, 26
	s_add_i32 s1, s0, s1
	s_ashr_i32 s2, s1, 6
	s_andn2_b32 s1, s1, 63
	s_sub_i32 s0, s0, s1
	s_bfe_i32 s1, s0, 0x80000
	s_bfe_u32 s1, s1, 0x3000c
	s_add_i32 s1, s0, s1
	s_bfe_i32 s3, s1, 0x80000
	s_and_b32 s1, s1, 0xf8
	s_sub_i32 s0, s0, s1
	s_sext_i32_i16 s3, s3
	s_sext_i32_i8 s0, s0
	s_ashr_i32 s1, s3, 3
	s_and_b32 s3, s0, 1
	s_lshl_b32 s0, s0, 3
	s_and_b32 s0, s0, 0x7ffffff0
	s_add_i32 s0, s0, s2
	s_lshl_b32 s0, s0, 1
	s_or_b32 s30, s0, s3
	s_lshl_b32 s0, s2, 3
	v_and_b32_e32 v6, 32, v0
	s_add_i32 s28, s0, s1
	s_lshr_b32 s8, s10, 6
	v_bitop3_b32 v10, v3, v6, 48 bitop3:0x6c
	v_and_b32_e32 v11, 64, v0
	s_ashr_i32 s31, s30, 31
	s_ashr_i32 s29, s28, 31
	s_lshr_b32 s11, s10, 8
	s_lshl_b32 s43, s8, 10
	v_or_b32_e32 v3, v10, v11
	s_lshl_b64 s[0:1], s[30:31], 20
	s_lshl_b64 s[2:3], s[28:29], 20
	s_waitcnt vmcnt(0)
	v_lshl_or_b32 v130, v4, 12, v3
	v_lshrrev_b32_e32 v4, 3, v0
	s_add_u32 s36, s41, s2
	v_and_or_b32 v2, v4, 32, v2
	s_addc_u32 s37, s42, s3
	s_add_i32 s29, s43, 0
	v_lshl_or_b32 v132, v2, 12, v3
	s_add_i32 m0, s29, 0x10000
	v_lshl_or_b32 v128, v5, 12, v3
	global_load_lds_dwordx4 v132, s[36:37]
	s_add_i32 m0, s29, 0x12000
	s_add_u32 s2, s36, 0x80000
	global_load_lds_dwordx4 v128, s[36:37]
	s_addc_u32 s3, s37, 0
	s_add_i32 m0, s29, 0x14000
	v_and_or_b32 v2, v4, 48, v13
	global_load_lds_dwordx4 v132, s[2:3]
	s_add_i32 m0, s29, 0x16000
	s_add_u32 s34, s33, s0
	s_addc_u32 s35, s40, s1
	s_add_i32 s31, s29, 0x2000
	v_lshl_or_b32 v134, v2, 12, v3
	global_load_lds_dwordx4 v128, s[2:3]
	s_mov_b32 m0, s29
	s_add_u32 s0, s34, 0x80000
	global_load_lds_dwordx4 v134, s[34:35]
	s_mov_b32 m0, s31
	s_addc_u32 s1, s35, 0
	s_add_i32 s44, s29, 0x4000
	global_load_lds_dwordx4 v130, s[34:35]
	s_mov_b32 m0, s44
	s_add_i32 s45, s29, 0x6000
	global_load_lds_dwordx4 v134, s[0:1]
	s_mov_b32 m0, s45
	v_mov_b32_e32 v137, 0
	global_load_lds_dwordx4 v130, s[0:1]
	v_mov_b32_e32 v133, v137
	v_mov_b32_e32 v129, v137
	v_mov_b32_e32 v135, v137
	v_mov_b32_e32 v131, v137
	s_cmp_eq_u32 s11, 1
	s_mov_b32 s46, 0
	v_lshl_add_u64 v[8:9], s[36:37], 0, v[132:133]
	v_lshl_add_u64 v[4:5], s[36:37], 0, v[128:129]
	s_mov_b64 s[0:1], 0x80000
	v_lshl_add_u64 v[2:3], s[34:35], 0, v[134:135]
	s_cselect_b64 s[2:3], -1, 0
	s_cmp_lg_u32 s11, 1
	v_lshl_add_u64 v[6:7], s[34:35], 0, v[130:131]
	s_cbranch_scc1 .LBB0_1343
	s_barrier

; #define PG8_STAGE(bufoff, gbase, voff) do { _Pragma("unroll") for (int _i = 0; _i < 2; ++_i) \
;         __builtin_amdgcn_global_load_lds((const unsigned*)((const char*)(gbase) + (voff)[_i]), (PG8_LAS unsigned*)(lds + (bufoff) + ldsw + _i * 8192), 16, 0, 0); } while (0)
; #define PG8_LDA(dst, b, h) do { _Pragma("unroll") for (int m = 0; m < 4; ++m) _Pragma("unroll") for (int k = 0; k < 2; ++k) dst[m][k] = *(const PG8_LAS bf16x8*)(lds + PG8_SA(b, h) + aoff + m * 2048 + k * 1024); } while (0)
; #define PG8_LDB(dst, b, h) do { _Pragma("unroll") for (int n = 0; n < 2; ++n) _Pragma("unroll") for (int k = 0; k < 2; ++k) dst[n][k] = *(const PG8_LAS bf16x8*)(lds + PG8_SB(b, h) + boff + n * 2048 + k * 1024); } while (0)
; #define PG8_MMA(ai, bj, At, Bt) do { __builtin_amdgcn_s_setprio(1); _Pragma("unroll") for (int m = 0; m < 4; ++m) _Pragma("unroll") for (int n = 0; n < 2; ++n) _Pragma("unroll") for (int k = 0; k < 2; ++k) \
;         acc[ai][bj][m][n] = __builtin_amdgcn_mfma_f32_16x16x32_bf16(Bt[n][k], At[m][k], acc[ai][bj][m][n], 0, 0, 0); __builtin_amdgcn_s_setprio(0); } while (0)
; #define PG8_WAIT_V(n) asm volatile("s_waitcnt vmcnt(" #n ")" ::: "memory")
; #define PG8_WAIT_L(n) asm volatile("s_waitcnt lgkmcnt(" #n ")" ::: "memory")
; #define PG8_BAR __builtin_amdgcn_s_barrier()
; #define PG8_SCHED __builtin_amdgcn_sched_barrier(0)
; #define PG8_STAGE(bufoff, gbase, voff) do { _Pragma("unroll") for (int _i = 0; _i < 2; ++_i) \
;         __builtin_amdgcn_global_load_lds((const unsigned*)((const char*)(gbase) + (voff)[_i]), (PG8_LAS unsigned*)(lds + (bufoff) + ldsw + _i * 8192), 16, 0, 0); } while (0)
; #define PG8_LDA(dst, b, h) do { _Pragma("unroll") for (int m = 0; m < 4; ++m) _Pragma("unroll") for (int k = 0; k < 2; ++k) dst[m][k] = *(const PG8_LAS bf16x8*)(lds + PG8_SA(b, h) + aoff + m * 2048 + k * 1024); } while (0)
; #define PG8_WAIT_V(n) asm volatile("s_waitcnt vmcnt(" #n ")" ::: "memory")
; template <class Epi, class Sched, bool ALIGN_EPI = false, bool SP2 = false>
; __device__ __forceinline__ void gemm_phase(PG8_LAS unsigned char* lds, const Gemm g, const Sched& S, const Epi& E) {
;     ...
;             PG8_LDB(B0, 0, 0); PG8_LDB(B1, 0, 1); PG8_SCHED; PG8_LDA(At, 0, 0); PG8_STAGE(PG8_SA(1, 1), a1 + hstep, voffA);
;             PG8_WAIT_V(8); PG8_WAIT_L(0); PG8_BAR; PG8_MMA(0, 0, At, B0); PG8_MMA(0, 1, At, B1); PG8_BAR; PG8_SCHED;
.LBB0_1349:
	ds_read_b128 v[152:155], v148
	ds_read_b128 v[156:159], v148 offset:1024
	ds_read_b128 v[160:163], v148 offset:2048
	ds_read_b128 v[164:167], v148 offset:3072
	ds_read_b128 v[168:171], v149
	ds_read_b128 v[172:175], v149 offset:1024
	ds_read_b128 v[176:179], v149 offset:2048
	ds_read_b128 v[180:183], v149 offset:3072
	s_add_u32 s36, s34, 0xfff80080
	s_addc_u32 s37, s35, -1
	s_cmp_eq_u32 s59, 28
	s_cselect_b32 s39, s19, s37
	s_cselect_b32 s38, s55, s36
	s_cselect_b32 s37, s21, s58
	s_cselect_b32 s36, s56, s57
	v_lshl_add_u64 v[144:145], s[34:35], 0, v[138:139]
	s_add_i32 m0, s29, 0xc000
	ds_read_b128 v[188:191], v150
	ds_read_b128 v[192:195], v150 offset:1024
	ds_read_b128 v[196:199], v150 offset:2048
	ds_read_b128 v[200:203], v150 offset:3072
	ds_read_b128 v[204:207], v150 offset:4096
	ds_read_b128 v[208:211], v150 offset:5120
	ds_read_b128 v[212:215], v150 offset:6144
	ds_read_b128 v[216:219], v150 offset:7168
	global_load_lds_dwordx4 v[144:145], off
	v_lshl_add_u64 v[144:145], s[34:35], 0, v[140:141]
	s_add_i32 m0, s29, 0xe000
	s_nop 0
	global_load_lds_dwordx4 v[144:145], off
	s_cmp_eq_u32 s100, 0
	s_cbranch_scc1 .Lllw11_a0
	s_waitcnt vmcnt(8)
.Lllw11_a0:
	s_waitcnt lgkmcnt(0)
	s_barrier
	s_setprio 1
	s_waitcnt lgkmcnt(0)
	v_mfma_f32_16x16x32_bf16 v[124:127], v[152:155], v[188:191], v[124:127]
	v_mfma_f32_16x16x32_bf16 v[120:123], v[160:163], v[188:191], v[120:123]
	v_mfma_f32_16x16x32_bf16 v[116:119], v[152:155], v[196:199], v[116:119]
	v_mfma_f32_16x16x32_bf16 v[112:115], v[160:163], v[196:199], v[112:115]
	v_mfma_f32_16x16x32_bf16 v[100:103], v[152:155], v[204:207], v[100:103]
	v_mfma_f32_16x16x32_bf16 v[96:99], v[160:163], v[204:207], v[96:99]
	v_mfma_f32_16x16x32_bf16 v[76:79], v[152:155], v[212:215], v[76:79]
	v_mfma_f32_16x16x32_bf16 v[72:75], v[160:163], v[212:215], v[72:75]
	v_mfma_f32_16x16x32_bf16 v[124:127], v[156:159], v[192:195], v[124:127]
	v_mfma_f32_16x16x32_bf16 v[120:123], v[164:167], v[192:195], v[120:123]
	v_mfma_f32_16x16x32_bf16 v[116:119], v[156:159], v[200:203], v[116:119]
	v_mfma_f32_16x16x32_bf16 v[112:115], v[164:167], v[200:203], v[112:115]
	v_mfma_f32_16x16x32_bf16 v[100:103], v[156:159], v[208:211], v[100:103]
	v_mfma_f32_16x16x32_bf16 v[96:99], v[164:167], v[208:211], v[96:99]
	v_mfma_f32_16x16x32_bf16 v[76:79], v[156:159], v[216:219], v[76:79]
	v_mfma_f32_16x16x32_bf16 v[72:75], v[164:167], v[216:219], v[72:75]
	s_setprio 0
	s_setprio 1
	v_mfma_f32_16x16x32_bf16 v[108:111], v[168:171], v[188:191], v[108:111]
	v_mfma_f32_16x16x32_bf16 v[104:107], v[176:179], v[188:191], v[104:107]
	v_mfma_f32_16x16x32_bf16 v[92:95], v[168:171], v[196:199], v[92:95]
	v_mfma_f32_16x16x32_bf16 v[88:91], v[176:179], v[196:199], v[88:91]
	v_mfma_f32_16x16x32_bf16 v[84:87], v[168:171], v[204:207], v[84:87]
	v_mfma_f32_16x16x32_bf16 v[80:83], v[176:179], v[204:207], v[80:83]
	v_mfma_f32_16x16x32_bf16 v[68:71], v[168:171], v[212:215], v[68:71]
	v_mfma_f32_16x16x32_bf16 v[64:67], v[176:179], v[212:215], v[64:67]
	v_mfma_f32_16x16x32_bf16 v[108:111], v[172:175], v[192:195], v[108:111]
	v_mfma_f32_16x16x32_bf16 v[104:107], v[180:183], v[192:195], v[104:107]
	v_mfma_f32_16x16x32_bf16 v[92:95], v[172:175], v[200:203], v[92:95]
	v_mfma_f32_16x16x32_bf16 v[88:91], v[180:183], v[200:203], v[88:91]
	v_mfma_f32_16x16x32_bf16 v[84:87], v[172:175], v[208:211], v[84:87]
	v_mfma_f32_16x16x32_bf16 v[80:83], v[180:183], v[208:211], v[80:83]
	v_mfma_f32_16x16x32_bf16 v[68:71], v[172:175], v[216:219], v[68:71]
	v_mfma_f32_16x16x32_bf16 v[64:67], v[180:183], v[216:219], v[64:67]
	s_setprio 0
	s_cmp_lg_u32 s100, 0
	s_cbranch_scc1 .Lllw11_b0
	s_waitcnt vmcnt(8)
; #define PG8_STAGE(bufoff, gbase, voff) do { _Pragma("unroll") for (int _i = 0; _i < 2; ++_i) \
;         __builtin_amdgcn_global_load_lds((const unsigned*)((const char*)(gbase) + (voff)[_i]), (PG8_LAS unsigned*)(lds + (bufoff) + ldsw + _i * 8192), 16, 0, 0); } while (0)
; #define PG8_LDA(dst, b, h) do { _Pragma("unroll") for (int m = 0; m < 4; ++m) _Pragma("unroll") for (int k = 0; k < 2; ++k) dst[m][k] = *(const PG8_LAS bf16x8*)(lds + PG8_SA(b, h) + aoff + m * 2048 + k * 1024); } while (0)
; #define PG8_LDB(dst, b, h) do { _Pragma("unroll") for (int n = 0; n < 2; ++n) _Pragma("unroll") for (int k = 0; k < 2; ++k) dst[n][k] = *(const PG8_LAS bf16x8*)(lds + PG8_SB(b, h) + boff + n * 2048 + k * 1024); } while (0)
; #define PG8_MMA(ai, bj, At, Bt) do { __builtin_amdgcn_s_setprio(1); _Pragma("unroll") for (int m = 0; m < 4; ++m) _Pragma("unroll") for (int n = 0; n < 2; ++n) _Pragma("unroll") for (int k = 0; k < 2; ++k) \
;         acc[ai][bj][m][n] = __builtin_amdgcn_mfma_f32_16x16x32_bf16(Bt[n][k], At[m][k], acc[ai][bj][m][n], 0, 0, 0); __builtin_amdgcn_s_setprio(0); } while (0)
; #define PG8_WAIT_V(n) asm volatile("s_waitcnt vmcnt(" #n ")" ::: "memory")
; #define PG8_WAIT_L(n) asm volatile("s_waitcnt lgkmcnt(" #n ")" ::: "memory")
; #define PG8_BAR __builtin_amdgcn_s_barrier()
; #define PG8_SCHED __builtin_amdgcn_sched_barrier(0)
; #define PG8_STAGE(bufoff, gbase, voff) do { _Pragma("unroll") for (int _i = 0; _i < 2; ++_i) \
;         __builtin_amdgcn_global_load_lds((const unsigned*)((const char*)(gbase) + (voff)[_i]), (PG8_LAS unsigned*)(lds + (bufoff) + ldsw + _i * 8192), 16, 0, 0); } while (0)
; #define PG8_BAR __builtin_amdgcn_s_barrier()
; template <class Epi, class Sched, bool ALIGN_EPI = false, bool SP2 = false>
; __device__ __forceinline__ void gemm_phase(PG8_LAS unsigned char* lds, const Gemm g, const Sched& S, const Epi& E) {
;     ...
;             PG8_WAIT_V(8); PG8_WAIT_L(0); PG8_BAR; PG8_MMA(0, 0, At, B0); PG8_MMA(0, 1, At, B1); PG8_BAR; PG8_SCHED;
;             PG8_LDA(At, 0, 1); PG8_STAGE(PG8_SB(0, 0), b2, voffB); PG8_STAGE(PG8_SB(0, 1), b2 + hstep, voffB); PG8_STAGE(PG8_SA(0, 0), a2, voffA);
;             PG8_WAIT_V(8); PG8_WAIT_L(0); PG8_BAR; PG8_MMA(1, 0, At, B0); PG8_MMA(1, 1, At, B1); PG8_BAR; PG8_SCHED;
;             PG8_LDB(B0, 1, 0); PG8_LDB(B1, 1, 1); PG8_SCHED; PG8_LDA(At, 1, 0); PG8_STAGE(PG8_SA(0, 1), a2 + hstep, voffA);
.Lllw11_b0:
	s_barrier
	s_add_i32 s60, s49, s43
	v_lshl_add_u64 v[144:145], s[36:37], 0, v[132:133]
	s_mov_b32 m0, s60
	ds_read_b128 v[188:191], v150 offset:16384
	ds_read_b128 v[192:195], v150 offset:17408
	ds_read_b128 v[196:199], v150 offset:18432
	ds_read_b128 v[200:203], v150 offset:19456
	ds_read_b128 v[204:207], v150 offset:20480
	ds_read_b128 v[208:211], v150 offset:21504
	ds_read_b128 v[212:215], v150 offset:22528
	ds_read_b128 v[216:219], v150 offset:23552
	global_load_lds_dwordx4 v[144:145], off
	s_add_i32 m0, s60, 0x2000
	s_add_u32 s60, s36, 0x80000
	v_lshl_add_u64 v[184:185], s[36:37], 0, v[128:129]
	s_addc_u32 s61, s37, 0
	s_add_i32 s62, s50, s43
	global_load_lds_dwordx4 v[184:185], off
	v_lshl_add_u64 v[220:221], s[60:61], 0, v[132:133]
	s_mov_b32 m0, s62
	v_lshl_add_u64 v[222:223], s[38:39], 0, v[130:131]
	global_load_lds_dwordx4 v[220:221], off
	v_lshl_add_u64 v[220:221], s[60:61], 0, v[128:129]
	s_add_i32 m0, s62, 0x2000
	s_nop 0
	global_load_lds_dwordx4 v[220:221], off
	v_lshl_add_u64 v[220:221], s[38:39], 0, v[134:135]
	s_mov_b32 m0, s29
	s_nop 0
	global_load_lds_dwordx4 v[220:221], off
	s_mov_b32 m0, s31
	s_nop 0
	global_load_lds_dwordx4 v[222:223], off
	s_cmp_eq_u32 s100, 0
	s_cbranch_scc1 .Lllw11_a1
	s_waitcnt vmcnt(8)
.Lllw11_a1:
	s_waitcnt lgkmcnt(0)
	s_barrier
	s_setprio 1
	s_waitcnt lgkmcnt(0)
	v_mfma_f32_16x16x32_bf16 v[60:63], v[152:155], v[188:191], v[60:63]
	v_mfma_f32_16x16x32_bf16 v[56:59], v[160:163], v[188:191], v[56:59]
	v_mfma_f32_16x16x32_bf16 v[52:55], v[152:155], v[196:199], v[52:55]
	v_mfma_f32_16x16x32_bf16 v[44:47], v[160:163], v[196:199], v[44:47]
	v_mfma_f32_16x16x32_bf16 v[36:39], v[152:155], v[204:207], v[36:39]
	v_mfma_f32_16x16x32_bf16 v[28:31], v[160:163], v[204:207], v[28:31]
	v_mfma_f32_16x16x32_bf16 v[20:23], v[152:155], v[212:215], v[20:23]
	v_mfma_f32_16x16x32_bf16 v[12:15], v[160:163], v[212:215], v[12:15]
	v_mfma_f32_16x16x32_bf16 v[60:63], v[156:159], v[192:195], v[60:63]
	v_mfma_f32_16x16x32_bf16 v[56:59], v[164:167], v[192:195], v[56:59]
	v_mfma_f32_16x16x32_bf16 v[52:55], v[156:159], v[200:203], v[52:55]
	v_mfma_f32_16x16x32_bf16 v[44:47], v[164:167], v[200:203], v[44:47]
	v_mfma_f32_16x16x32_bf16 v[36:39], v[156:159], v[208:211], v[36:39]
	v_mfma_f32_16x16x32_bf16 v[28:31], v[164:167], v[208:211], v[28:31]
	v_mfma_f32_16x16x32_bf16 v[20:23], v[156:159], v[216:219], v[20:23]
	v_mfma_f32_16x16x32_bf16 v[12:15], v[164:167], v[216:219], v[12:15]
	s_setprio 0
	s_setprio 1
	v_mfma_f32_16x16x32_bf16 v[48:51], v[168:171], v[188:191], v[48:51]
	v_mfma_f32_16x16x32_bf16 v[40:43], v[176:179], v[188:191], v[40:43]
	v_mfma_f32_16x16x32_bf16 v[32:35], v[168:171], v[196:199], v[32:35]
	v_mfma_f32_16x16x32_bf16 v[24:27], v[176:179], v[196:199], v[24:27]
	v_mfma_f32_16x16x32_bf16 v[16:19], v[168:171], v[204:207], v[16:19]
	v_mfma_f32_16x16x32_bf16 v[8:11], v[176:179], v[204:207], v[8:11]
	v_mfma_f32_16x16x32_bf16 v[4:7], v[168:171], v[212:215], v[4:7]
	v_mfma_f32_16x16x32_bf16 v[0:3], v[176:179], v[212:215], v[0:3]
	v_mfma_f32_16x16x32_bf16 v[48:51], v[172:175], v[192:195], v[48:51]
	v_mfma_f32_16x16x32_bf16 v[40:43], v[180:183], v[192:195], v[40:43]
	v_mfma_f32_16x16x32_bf16 v[32:35], v[172:175], v[200:203], v[32:35]
	v_mfma_f32_16x16x32_bf16 v[24:27], v[180:183], v[200:203], v[24:27]
	v_mfma_f32_16x16x32_bf16 v[16:19], v[172:175], v[208:211], v[16:19]
	v_mfma_f32_16x16x32_bf16 v[8:11], v[180:183], v[208:211], v[8:11]
	v_mfma_f32_16x16x32_bf16 v[4:7], v[172:175], v[216:219], v[4:7]
	v_mfma_f32_16x16x32_bf16 v[0:3], v[180:183], v[216:219], v[0:3]
	s_setprio 0
	s_cmp_lg_u32 s100, 0
	s_cbranch_scc1 .Lllw11_b1
	s_waitcnt vmcnt(8)
.Lllw11_b1:
	s_barrier
	s_add_i32 s60, 0, 0x18000
	v_add_u32_e32 v136, s60, v146
	s_add_i32 s61, 0, 0x1c000
	ds_read_b128 v[152:155], v136
	ds_read_b128 v[156:159], v136 offset:1024
	ds_read_b128 v[160:163], v136 offset:2048
	ds_read_b128 v[164:167], v136 offset:3072
	v_add_u32_e32 v136, s61, v146
	ds_read_b128 v[168:171], v136
	ds_read_b128 v[172:175], v136 offset:1024
	ds_read_b128 v[176:179], v136 offset:2048
	ds_read_b128 v[180:183], v136 offset:3072
	s_add_u32 s38, s38, 0x80000
	s_addc_u32 s39, s39, 0
	s_mov_b32 m0, s44
	v_lshl_add_u64 v[224:225], s[38:39], 0, v[134:135]
	ds_read_b128 v[188:191], v150 offset:32768
	ds_read_b128 v[192:195], v150 offset:33792
	ds_read_b128 v[196:199], v150 offset:34816
	ds_read_b128 v[200:203], v150 offset:35840
	ds_read_b128 v[204:207], v150 offset:36864
	ds_read_b128 v[208:211], v150 offset:37888
	ds_read_b128 v[212:215], v150 offset:38912
	ds_read_b128 v[216:219], v150 offset:39936
	global_load_lds_dwordx4 v[224:225], off
	v_lshl_add_u64 v[224:225], s[38:39], 0, v[130:131]
	s_mov_b32 m0, s45
	s_nop 0
	global_load_lds_dwordx4 v[224:225], off
	s_cmp_eq_u32 s100, 0
	s_cbranch_scc1 .Lllw11_a2
	s_waitcnt vmcnt(8)

; #define PG8_STAGE(bufoff, gbase, voff) do { _Pragma("unroll") for (int _i = 0; _i < 2; ++_i) \
;         __builtin_amdgcn_global_load_lds((const unsigned*)((const char*)(gbase) + (voff)[_i]), (PG8_LAS unsigned*)(lds + (bufoff) + ldsw + _i * 8192), 16, 0, 0); } while (0)
; #define PG8_LDA(dst, b, h) do { _Pragma("unroll") for (int m = 0; m < 4; ++m) _Pragma("unroll") for (int k = 0; k < 2; ++k) dst[m][k] = *(const PG8_LAS bf16x8*)(lds + PG8_SA(b, h) + aoff + m * 2048 + k * 1024); } while (0)
; #define PG8_MMA(ai, bj, At, Bt) do { __builtin_amdgcn_s_setprio(1); _Pragma("unroll") for (int m = 0; m < 4; ++m) _Pragma("unroll") for (int n = 0; n < 2; ++n) _Pragma("unroll") for (int k = 0; k < 2; ++k) \
;         acc[ai][bj][m][n] = __builtin_amdgcn_mfma_f32_16x16x32_bf16(Bt[n][k], At[m][k], acc[ai][bj][m][n], 0, 0, 0); __builtin_amdgcn_s_setprio(0); } while (0)
; #define PG8_WAIT_V(n) asm volatile("s_waitcnt vmcnt(" #n ")" ::: "memory")
; #define PG8_WAIT_L(n) asm volatile("s_waitcnt lgkmcnt(" #n ")" ::: "memory")
; #define PG8_BAR __builtin_amdgcn_s_barrier()
; #define PG8_SCHED __builtin_amdgcn_sched_barrier(0)
; #define PG8_STAGE(bufoff, gbase, voff) do { _Pragma("unroll") for (int _i = 0; _i < 2; ++_i) \
;         __builtin_amdgcn_global_load_lds((const unsigned*)((const char*)(gbase) + (voff)[_i]), (PG8_LAS unsigned*)(lds + (bufoff) + ldsw + _i * 8192), 16, 0, 0); } while (0)
; #define PG8_LDA(dst, b, h) do { _Pragma("unroll") for (int m = 0; m < 4; ++m) _Pragma("unroll") for (int k = 0; k < 2; ++k) dst[m][k] = *(const PG8_LAS bf16x8*)(lds + PG8_SA(b, h) + aoff + m * 2048 + k * 1024); } while (0)
; #define PG8_WAIT_V(n) asm volatile("s_waitcnt vmcnt(" #n ")" ::: "memory")
; #define PG8_WAIT_L(n) asm volatile("s_waitcnt lgkmcnt(" #n ")" ::: "memory")
; #define PG8_BAR __builtin_amdgcn_s_barrier()
; #define PG8_SCHED __builtin_amdgcn_sched_barrier(0)
; template <class Epi, class Sched, bool ALIGN_EPI = false, bool SP2 = false>
; __device__ __forceinline__ void gemm_phase(PG8_LAS unsigned char* lds, const Gemm g, const Sched& S, const Epi& E) {
;     ...
;             PG8_LDA(At, 1, 1); PG8_STAGE(PG8_SB(1, 0), b3, voffB); PG8_STAGE(PG8_SB(1, 1), b3 + hstep, voffB); PG8_STAGE(PG8_SA(1, 0), a3, voffA);
;             PG8_WAIT_V(8); PG8_WAIT_L(0); PG8_BAR; PG8_MMA(1, 0, At, B0); PG8_MMA(1, 1, At, B1); PG8_BAR; PG8_SCHED;
.Lllw11_b2:
	s_barrier
	s_add_i32 s38, s60, s43
	v_lshl_add_u64 v[144:145], v[144:145], 0, s[8:9]
	s_mov_b32 m0, s38
	ds_read_b128 v[188:191], v150 offset:49152
	ds_read_b128 v[192:195], v150 offset:50176
	ds_read_b128 v[196:199], v150 offset:51200
	ds_read_b128 v[200:203], v150 offset:52224
	ds_read_b128 v[204:207], v150 offset:53248
	ds_read_b128 v[208:211], v150 offset:54272
	ds_read_b128 v[212:215], v150 offset:55296
	ds_read_b128 v[216:219], v150 offset:56320
	global_load_lds_dwordx4 v[144:145], off
	s_add_i32 m0, s38, 0x2000
	s_add_u32 s36, s36, 0x80080
	v_lshl_add_u64 v[144:145], v[184:185], 0, s[8:9]
	s_addc_u32 s37, s37, 0
	s_add_i32 s38, s61, s43
	global_load_lds_dwordx4 v[144:145], off
	v_lshl_add_u64 v[144:145], s[36:37], 0, v[132:133]
	s_mov_b32 m0, s38
	s_nop 0
	global_load_lds_dwordx4 v[144:145], off
	v_lshl_add_u64 v[144:145], s[36:37], 0, v[128:129]
	s_add_i32 m0, s38, 0x2000
	s_nop 0
	global_load_lds_dwordx4 v[144:145], off
	v_lshl_add_u64 v[144:145], v[220:221], 0, s[8:9]
	s_mov_b32 m0, s47
	s_nop 0
	global_load_lds_dwordx4 v[144:145], off
	v_lshl_add_u64 v[144:145], v[222:223], 0, s[8:9]
	s_mov_b32 m0, s48
	s_nop 0
	global_load_lds_dwordx4 v[144:145], off
	s_cmp_eq_u32 s100, 0
	s_cbranch_scc1 .Lllw11_a3
	s_waitcnt vmcnt(8)

; #define PG8_MMA(ai, bj, At, Bt) do { __builtin_amdgcn_s_setprio(1); _Pragma("unroll") for (int m = 0; m < 4; ++m) _Pragma("unroll") for (int n = 0; n < 2; ++n) _Pragma("unroll") for (int k = 0; k < 2; ++k) \
;         acc[ai][bj][m][n] = __builtin_amdgcn_mfma_f32_16x16x32_bf16(Bt[n][k], At[m][k], acc[ai][bj][m][n], 0, 0, 0); __builtin_amdgcn_s_setprio(0); } while (0)
; #define PG8_WAIT_V(n) asm volatile("s_waitcnt vmcnt(" #n ")" ::: "memory")
; #define PG8_WAIT_L(n) asm volatile("s_waitcnt lgkmcnt(" #n ")" ::: "memory")
; #define PG8_BAR __builtin_amdgcn_s_barrier()
; #define PG8_SCHED __builtin_amdgcn_sched_barrier(0)
; #define PG8_MMA(ai, bj, At, Bt) do { __builtin_amdgcn_s_setprio(1); _Pragma("unroll") for (int m = 0; m < 4; ++m) _Pragma("unroll") for (int n = 0; n < 2; ++n) _Pragma("unroll") for (int k = 0; k < 2; ++k) \
;         acc[ai][bj][m][n] = __builtin_amdgcn_mfma_f32_16x16x32_bf16(Bt[n][k], At[m][k], acc[ai][bj][m][n], 0, 0, 0); __builtin_amdgcn_s_setprio(0); } while (0)
; #define PG8_WAIT_V(n) asm volatile("s_waitcnt vmcnt(" #n ")" ::: "memory")
; #define PG8_WAIT_L(n) asm volatile("s_waitcnt lgkmcnt(" #n ")" ::: "memory")
; #define PG8_BAR __builtin_amdgcn_s_barrier()
; #define PG8_SCHED __builtin_amdgcn_sched_barrier(0)
; template <class Epi, class Sched, bool ALIGN_EPI = false, bool SP2 = false>
; __device__ __forceinline__ void gemm_phase(PG8_LAS unsigned char* lds, const Gemm g, const Sched& S, const Epi& E) {
;     ...
;             PG8_WAIT_V(8); PG8_WAIT_L(0); PG8_BAR; PG8_MMA(1, 0, At, B0); PG8_MMA(1, 1, At, B1); PG8_BAR; PG8_SCHED;
;             } else {
.Lllw11_b3:
	s_barrier
	s_add_i32 s59, s59, 2
	s_add_u32 s34, s34, 0x100
	s_addc_u32 s35, s35, 0
	s_add_u32 s57, s57, 0x100
	s_addc_u32 s58, s58, 0
	s_cmp_gt_u32 s59, 29
	s_cbranch_scc0 .LBB0_1349
	s_and_b64 vcc, exec, s[10:11]
	s_cbranch_vccz .LBB0_1352
	s_barrier
